# attention PV blocks: each transition s_waitcnt lgkmcnt(0) moved below the MFMA(s) whose operands were already drained (36 sites, 12 in the hot loops)
# speedup vs baseline: 1.0036x; 1.0036x over previous
.Lcw_a_done:
	s_mov_b32 s1, s97
	s_mov_b32 m0, s86
	s_add_i32 s5, s0, 0xffff2000
	ds_read_b128 v[0:3], v190 offset:32768
	ds_read_b128 v[112:115], v190 offset:40960
	buffer_load_dwordx4 v191, s[68:71], s5 offen lds
	ds_read_b128 v[4:7], v189 offset:32768
	ds_read_b128 v[116:119], v189 offset:40960
	s_add_i32 s6, s0, 0xffff4000
	s_mov_b32 m0, s85
	s_waitcnt lgkmcnt(3)
	v_mfma_f32_32x32x16_f16 v[80:95], v[0:3], v[156:159], -0.5
	s_add_i32 s7, s0, 0xffff6000
	buffer_load_dwordx4 v191, s[68:71], s6 offen lds
	s_waitcnt lgkmcnt(1)
	v_mfma_f32_32x32x16_f16 v[80:95], v[4:7], v[152:155], v[80:95]
	v_mfma_f32_32x32x16_f16 v[0:15], v[112:115], v[156:159], -0.5
	ds_read_b128 v[112:115], v188 offset:32768
	s_mov_b32 m0, s84
	s_add_i32 s9, s0, 0xffff8000
	s_add_i32 s10, s0, 0xfffea000
	v_exp_f32_e32 v182, v100
	v_exp_f32_e32 v183, v101
	s_waitcnt lgkmcnt(1)
	v_mfma_f32_32x32x16_f16 v[0:15], v[116:119], v[152:155], v[0:15]
	ds_read_b128 v[116:119], v188 offset:40960
	buffer_load_dwordx4 v191, s[68:71], s7 offen lds
	s_mov_b32 m0, s83
	v_exp_f32_e32 v192, v106
	v_exp_f32_e32 v193, v107
	v_exp_f32_e32 v194, v108
	v_exp_f32_e32 v111, v111
	s_waitcnt lgkmcnt(1)
	v_mfma_f32_32x32x16_f16 v[80:95], v[112:115], v[148:151], v[80:95]
	ds_read_b128 v[112:115], v187 offset:32768
	ds_read_b128 v[120:123], v187 offset:40960
	buffer_load_dwordx4 v191, s[68:71], s9 offen lds
	s_mov_b32 m0, s90
	ds_read_b128 v[124:127], v190 offset:32896
	ds_read_b128 v[162:165], v190 offset:41088
	buffer_load_dwordx4 v186, s[72:75], s10 offen lds
	s_add_i32 s10, s0, 0xfffec000
	s_mov_b32 m0, s89
	s_waitcnt lgkmcnt(4)
	v_mfma_f32_32x32x16_f16 v[0:15], v[116:119], v[148:151], v[0:15]
	ds_read_b128 v[116:119], v189 offset:32896
	ds_read_b128 v[166:169], v189 offset:41088
	buffer_load_dwordx4 v186, s[72:75], s10 offen lds
	s_add_i32 s10, s0, 0xfffee000
	s_mov_b32 m0, s88
	v_cvt_pk_f16_f32 v100, v218, v219
	v_cvt_pk_f16_f32 v101, v220, v221
	v_cvt_pk_f16_f32 v106, v182, v183
	s_waitcnt lgkmcnt(5)
	v_mfma_f32_32x32x16_f16 v[80:95], v[112:115], v[144:147], v[80:95]
	ds_read_b128 v[112:115], v188 offset:32896
	ds_read_b128 v[170:173], v188 offset:41088
	buffer_load_dwordx4 v186, s[72:75], s10 offen lds
	s_add_i32 s10, s0, 0xffff0000
	s_mov_b32 m0, s87
	ds_read_b128 v[174:177], v187 offset:32896
	ds_read_b128 v[178:181], v187 offset:41088
	buffer_load_dwordx4 v186, s[72:75], s10 offen lds
	s_waitcnt lgkmcnt(8)
	v_mfma_f32_32x32x16_f16 v[0:15], v[120:123], v[144:147], v[0:15]
	v_exp_f32_e32 v120, v96
	v_add_f32_e32 v96, 0, v210
	v_add_f32_e32 v96, v211, v96
	v_add_f32_e32 v96, v212, v96
	v_add_f32_e32 v96, v213, v96
	v_add_f32_e32 v96, v214, v96
	v_add_f32_e32 v96, v215, v96
	s_waitcnt lgkmcnt(7)
	v_mfma_f32_32x32x16_f16 v[80:95], v[124:127], v[140:143], v[80:95]
	v_add_f32_e32 v96, v216, v96
	v_add_f32_e32 v96, v217, v96
	v_add_f32_e32 v96, v218, v96
	v_add_f32_e32 v96, v219, v96
	v_add_f32_e32 v96, v220, v96
	v_add_f32_e32 v96, v221, v96
	v_add_f32_e32 v96, v222, v96
	v_exp_f32_e32 v121, v97
	s_waitcnt lgkmcnt(6)
	v_mfma_f32_32x32x16_f16 v[0:15], v[162:165], v[140:143], v[0:15]
	v_add_f32_e32 v96, v223, v96
	v_exp_f32_e32 v122, v98
	v_add_f32_e32 v96, v224, v96
	v_exp_f32_e32 v123, v99
	v_add_f32_e32 v96, v225, v96
	v_add_f32_e32 v96, v120, v96
	v_add_f32_e32 v96, v121, v96
	s_waitcnt lgkmcnt(5)
	v_mfma_f32_32x32x16_f16 v[80:95], v[116:119], v[136:139], v[80:95]
	v_exp_f32_e32 v124, v102
	v_add_f32_e32 v96, v122, v96
	v_exp_f32_e32 v125, v103
	v_add_f32_e32 v96, v123, v96
	v_exp_f32_e32 v126, v104
	v_add_f32_e32 v96, v182, v96
	v_exp_f32_e32 v127, v105
	s_waitcnt lgkmcnt(4)
	v_mfma_f32_32x32x16_f16 v[0:15], v[166:169], v[136:139], v[0:15]
	v_add_f32_e32 v96, v183, v96
	v_add_f32_e32 v96, v124, v96
	v_add_f32_e32 v96, v125, v96
	v_add_f32_e32 v96, v126, v96
	v_exp_f32_e32 v162, v109
	v_add_f32_e32 v96, v127, v96
	v_exp_f32_e32 v163, v110
	s_waitcnt lgkmcnt(3)
	v_mfma_f32_32x32x16_f16 v[80:95], v[112:115], v[132:135], v[80:95]
	v_add_f32_e32 v96, v192, v96
	v_add_f32_e32 v96, v193, v96
	v_add_f32_e32 v96, v194, v96
	v_add_f32_e32 v96, v162, v96
	v_add_f32_e32 v96, v163, v96
	v_add_f32_e32 v96, v111, v96
	v_mov_b32_e32 v97, v96
	s_waitcnt lgkmcnt(2)
	v_mfma_f32_32x32x16_f16 v[0:15], v[170:173], v[132:135], v[0:15]
	v_permlane32_swap_b32_e32 v96, v97
	v_add_f32_e32 v96, v96, v97
	v_add_f32_e32 v185, v185, v96
	v_cvt_pk_f16_f32 v96, v210, v211
	v_cvt_pk_f16_f32 v97, v212, v213
	v_cvt_pk_f16_f32 v98, v214, v215
	s_waitcnt lgkmcnt(1)
	v_mfma_f32_32x32x16_f16 v[80:95], v[174:177], v[128:131], v[80:95]
	v_cvt_pk_f16_f32 v99, v216, v217
	v_cvt_pk_f16_f32 v102, v222, v223
	v_cvt_pk_f16_f32 v103, v224, v225
	v_cvt_pk_f16_f32 v104, v120, v121
	v_cvt_pk_f16_f32 v105, v122, v123
	v_cvt_pk_f16_f32 v107, v124, v125
	v_cvt_pk_f16_f32 v108, v126, v127
	v_cvt_pk_f16_f32 v109, v192, v193
	v_cvt_pk_f16_f32 v110, v194, v162
	v_cvt_pk_f16_f32 v111, v163, v111
	v_permlane32_swap_b32_e32 v96, v98
	v_permlane32_swap_b32_e32 v97, v99
	v_permlane32_swap_b32_e32 v100, v102
	v_permlane32_swap_b32_e32 v101, v103
	v_permlane32_swap_b32_e32 v104, v106
	v_permlane32_swap_b32_e32 v105, v107
	v_permlane32_swap_b32_e32 v108, v110
	v_permlane32_swap_b32_e32 v109, v111
	s_waitcnt lgkmcnt(0)
	v_mfma_f32_32x32x16_f16 v[0:15], v[178:181], v[128:131], v[0:15]
	ds_read_b64_tr_b16 v[112:113], v184 offset:0
	ds_read_b64_tr_b16 v[114:115], v184 offset:0x800
	ds_read_b64_tr_b16 v[116:117], v184 offset:0x1000
	ds_read_b64_tr_b16 v[118:119], v184 offset:0x1800
	ds_read_b64_tr_b16 v[120:121], v184 offset:0x2000
	ds_read_b64_tr_b16 v[122:123], v184 offset:0x2800
	ds_read_b64_tr_b16 v[124:125], v184 offset:0x3000
	ds_read_b64_tr_b16 v[126:127], v184 offset:0x3800
	s_waitcnt lgkmcnt(0)
	s_nop 0
	v_mfma_f32_32x32x16_f16 v[64:79], v[96:99], v[112:115], v[64:79]
	v_exp_f32_e32 v208, v80
	v_exp_f32_e32 v192, v81
	ds_read_b64_tr_b16 v[80:81], v184 offset:0x200
	v_exp_f32_e32 v193, v82
	v_exp_f32_e32 v194, v83
	ds_read_b64_tr_b16 v[82:83], v184 offset:0xa00
	ds_read_b64_tr_b16 v[112:113], v184 offset:0x1200
	v_mfma_f32_32x32x16_f16 v[64:79], v[100:103], v[116:119], v[64:79]
	ds_read_b64_tr_b16 v[114:115], v184 offset:0x1a00
	ds_read_b64_tr_b16 v[116:117], v184 offset:0x2200
	ds_read_b64_tr_b16 v[118:119], v184 offset:0x2a00
	v_mfma_f32_32x32x16_f16 v[64:79], v[104:107], v[120:123], v[64:79]
	ds_read_b64_tr_b16 v[120:121], v184 offset:0x3200
	ds_read_b64_tr_b16 v[122:123], v184 offset:0x3a00
	v_mfma_f32_32x32x16_f16 v[64:79], v[108:111], v[124:127], v[64:79]
	s_waitcnt lgkmcnt(0)
	v_mfma_f32_32x32x16_f16 v[48:63], v[96:99], v[80:83], v[48:63]
	ds_read_b64_tr_b16 v[80:81], v184 offset:0x400
	ds_read_b64_tr_b16 v[82:83], v184 offset:0xc00
	v_exp_f32_e32 v195, v84
	v_exp_f32_e32 v196, v85
	ds_read_b64_tr_b16 v[84:85], v184 offset:0x1400
	v_exp_f32_e32 v197, v86
	v_exp_f32_e32 v198, v87
	v_mfma_f32_32x32x16_f16 v[48:63], v[100:103], v[112:115], v[48:63]
	ds_read_b64_tr_b16 v[86:87], v184 offset:0x1c00
	ds_read_b64_tr_b16 v[112:113], v184 offset:0x2400
	ds_read_b64_tr_b16 v[114:115], v184 offset:0x2c00
	v_mfma_f32_32x32x16_f16 v[48:63], v[104:107], v[116:119], v[48:63]
	ds_read_b64_tr_b16 v[116:117], v184 offset:0x3400
	ds_read_b64_tr_b16 v[118:119], v184 offset:0x3c00
	v_mfma_f32_32x32x16_f16 v[48:63], v[108:111], v[120:123], v[48:63]
	s_waitcnt lgkmcnt(0)
	v_mfma_f32_32x32x16_f16 v[32:47], v[96:99], v[80:83], v[32:47]
	ds_read_b64_tr_b16 v[80:81], v184 offset:0x600
	ds_read_b64_tr_b16 v[82:83], v184 offset:0xe00
	v_exp_f32_e32 v199, v88
	v_exp_f32_e32 v200, v89
	v_exp_f32_e32 v201, v90
	v_exp_f32_e32 v202, v91
	v_mfma_f32_32x32x16_f16 v[32:47], v[100:103], v[84:87], v[32:47]
	ds_read_b64_tr_b16 v[84:85], v184 offset:0x1600
	ds_read_b64_tr_b16 v[86:87], v184 offset:0x1e00
	ds_read_b64_tr_b16 v[88:89], v184 offset:0x2600
	ds_read_b64_tr_b16 v[90:91], v184 offset:0x2e00
	v_mfma_f32_32x32x16_f16 v[32:47], v[104:107], v[112:115], v[32:47]
	ds_read_b64_tr_b16 v[112:113], v184 offset:0x3600
	ds_read_b64_tr_b16 v[114:115], v184 offset:0x3e00
	v_mfma_f32_32x32x16_f16 v[32:47], v[108:111], v[116:119], v[32:47]
	s_waitcnt lgkmcnt(0)
	v_mfma_f32_32x32x16_f16 v[16:31], v[96:99], v[80:83], v[16:31]
	v_exp_f32_e32 v203, v92
	v_exp_f32_e32 v204, v93
	v_exp_f32_e32 v205, v94
	v_exp_f32_e32 v206, v95
	s_waitcnt vmcnt(0) lgkmcnt(0)
	s_barrier
	v_mfma_f32_32x32x16_f16 v[16:31], v[100:103], v[84:87], v[16:31]
	v_mfma_f32_32x32x16_f16 v[16:31], v[104:107], v[88:91], v[16:31]
	v_mfma_f32_32x32x16_f16 v[16:31], v[108:111], v[112:115], v[16:31]
	s_cmp_gt_u32 s100, 8
	s_cbranch_scc1 .Lcw_b_done
	s_cmp_eq_u32 s100, 0
	s_cbranch_scc1 .Lcw_b_load
	v_cvt_pk_f16_f32 v252, v252, v253
	v_cvt_pk_f16_f32 v253, v254, v255
	v_lshrrev_b32_e32 v254, 1, v191
	global_store_dwordx2 v254, v[252:253], s[60:61]
	s_add_u32 s60, s60, 0x1000
	s_addc_u32 s61, s61, 0
	s_cmp_eq_u32 s100, 8
	s_cbranch_scc1 .Lcw_b_inc

.Lcw_b_done:
	s_mov_b32 m0, s91
	s_add_i32 s10, s0, 0xffffa000
	ds_read_b128 v[80:83], v190
	ds_read_b128 v[84:87], v190 offset:8192
	buffer_load_dwordx4 v191, s[68:71], s10 offen lds
	ds_read_b128 v[88:91], v189
	ds_read_b128 v[92:95], v189 offset:8192
	s_add_i32 s10, s0, 0xffffc000
	s_mov_b32 m0, s92
	s_waitcnt lgkmcnt(3)
	v_mfma_f32_32x32x16_f16 v[112:127], v[80:83], v[156:159], -0.5
	s_waitcnt lgkmcnt(2)
	v_mfma_f32_32x32x16_f16 v[96:111], v[84:87], v[156:159], -0.5
	buffer_load_dwordx4 v191, s[68:71], s10 offen lds
	ds_read_b128 v[80:83], v188
	ds_read_b128 v[84:87], v188 offset:8192
	s_waitcnt lgkmcnt(3)
	v_mfma_f32_32x32x16_f16 v[112:127], v[88:91], v[152:155], v[112:127]
	s_add_i32 s10, s0, 0xffffe000
	s_mov_b32 m0, s93
	s_nop 0
	buffer_load_dwordx4 v191, s[68:71], s10 offen lds
	s_mov_b32 m0, s94
	s_waitcnt lgkmcnt(1)
	v_mfma_f32_32x32x16_f16 v[112:127], v[80:83], v[148:151], v[112:127]
	ds_read_b128 v[80:83], v187
	ds_read_b128 v[88:91], v187 offset:8192
	buffer_load_dwordx4 v191, s[68:71], s0 offen lds
	s_mov_b32 m0, s3
	v_mfma_f32_32x32x16_f16 v[96:111], v[92:95], v[152:155], v[96:111]
	ds_read_b128 v[92:95], v190 offset:128
	ds_read_b128 v[162:165], v190 offset:8320
	buffer_load_dwordx4 v186, s[72:75], s5 offen lds
	s_mov_b32 m0, s82
	ds_read_b128 v[166:169], v189 offset:128
	ds_read_b128 v[170:173], v189 offset:8320
	buffer_load_dwordx4 v186, s[72:75], s6 offen lds
	s_mov_b32 m0, s81
	ds_read_b128 v[174:177], v188 offset:128
	ds_read_b128 v[178:181], v188 offset:8320
	buffer_load_dwordx4 v186, s[72:75], s7 offen lds
	s_mov_b32 m0, s80
	ds_read_b128 v[210:213], v187 offset:128
	ds_read_b128 v[214:217], v187 offset:8320
	buffer_load_dwordx4 v186, s[72:75], s9 offen lds
	s_waitcnt lgkmcnt(10)
	v_mfma_f32_32x32x16_f16 v[96:111], v[84:87], v[148:151], v[96:111]
	v_exp_f32_e32 v84, v4
	v_exp_f32_e32 v85, v5
	v_exp_f32_e32 v86, v6
	v_exp_f32_e32 v87, v7
	v_cvt_pk_f16_f32 v4, v199, v200
	v_cvt_pk_f16_f32 v5, v201, v202
	v_cvt_pk_f16_f32 v6, v203, v204
	s_waitcnt lgkmcnt(8)
	v_mfma_f32_32x32x16_f16 v[96:111], v[88:91], v[144:147], v[96:111]
	v_exp_f32_e32 v88, v8
	v_exp_f32_e32 v89, v9
	v_exp_f32_e32 v90, v10
	v_exp_f32_e32 v91, v11
	v_cvt_pk_f16_f32 v7, v205, v206
	v_cvt_pk_f16_f32 v10, v84, v85
	v_cvt_pk_f16_f32 v11, v86, v87
	v_mfma_f32_32x32x16_f16 v[112:127], v[80:83], v[144:147], v[112:127]
	v_exp_f32_e32 v80, v0
	v_add_f32_e32 v0, 0, v208
	v_add_f32_e32 v0, v192, v0
	v_add_f32_e32 v0, v193, v0
	v_add_f32_e32 v0, v194, v0
	v_add_f32_e32 v0, v195, v0
	v_add_f32_e32 v0, v196, v0
	s_waitcnt lgkmcnt(6)
	v_mfma_f32_32x32x16_f16 v[96:111], v[162:165], v[140:143], v[96:111]
	v_add_f32_e32 v0, v197, v0
	v_add_f32_e32 v0, v198, v0
	v_add_f32_e32 v0, v199, v0
	v_add_f32_e32 v0, v200, v0
	v_add_f32_e32 v0, v201, v0
	v_add_f32_e32 v0, v202, v0
	v_add_f32_e32 v0, v203, v0
	v_mfma_f32_32x32x16_f16 v[112:127], v[92:95], v[140:143], v[112:127]
	v_exp_f32_e32 v81, v1
	v_add_f32_e32 v0, v204, v0
	v_exp_f32_e32 v82, v2
	v_add_f32_e32 v0, v205, v0
	v_exp_f32_e32 v83, v3
	v_add_f32_e32 v0, v206, v0
	v_add_f32_e32 v0, v80, v0
	s_waitcnt lgkmcnt(4)
	v_mfma_f32_32x32x16_f16 v[96:111], v[170:173], v[136:139], v[96:111]
	v_add_f32_e32 v0, v81, v0
	v_add_f32_e32 v0, v82, v0
	v_add_f32_e32 v0, v83, v0
	v_add_f32_e32 v0, v84, v0
	v_add_f32_e32 v0, v85, v0
	v_add_f32_e32 v0, v86, v0
	v_add_f32_e32 v0, v87, v0
	v_mfma_f32_32x32x16_f16 v[112:127], v[166:169], v[136:139], v[112:127]
	v_exp_f32_e32 v92, v12
	v_add_f32_e32 v0, v88, v0
	v_exp_f32_e32 v93, v13
	v_add_f32_e32 v0, v89, v0
	v_exp_f32_e32 v94, v14
	v_add_f32_e32 v0, v90, v0
	v_exp_f32_e32 v95, v15
	s_waitcnt lgkmcnt(2)
	v_mfma_f32_32x32x16_f16 v[96:111], v[178:181], v[132:135], v[96:111]
	v_add_f32_e32 v0, v91, v0
	v_add_f32_e32 v0, v92, v0
	v_add_f32_e32 v0, v93, v0
	v_add_f32_e32 v0, v94, v0
	v_add_f32_e32 v0, v95, v0
	v_mov_b32_e32 v1, v0
	s_nop 1
	v_permlane32_swap_b32_e32 v0, v1
	v_mfma_f32_32x32x16_f16 v[112:127], v[174:177], v[132:135], v[112:127]
	v_add_f32_e32 v0, v0, v1
	v_add_f32_e32 v185, v185, v0
	v_cvt_pk_f16_f32 v0, v208, v192
	v_cvt_pk_f16_f32 v1, v193, v194
	v_cvt_pk_f16_f32 v2, v195, v196
	v_cvt_pk_f16_f32 v3, v197, v198
	v_cvt_pk_f16_f32 v8, v80, v81
	s_waitcnt lgkmcnt(0)
	v_mfma_f32_32x32x16_f16 v[96:111], v[214:217], v[128:131], v[96:111]
	v_cvt_pk_f16_f32 v9, v82, v83
	v_cvt_pk_f16_f32 v12, v88, v89
	v_cvt_pk_f16_f32 v13, v90, v91
	v_cvt_pk_f16_f32 v14, v92, v93
	v_cvt_pk_f16_f32 v15, v94, v95
	v_permlane32_swap_b32_e32 v0, v2
	v_mfma_f32_32x32x16_f16 v[112:127], v[210:213], v[128:131], v[112:127]
	v_permlane32_swap_b32_e32 v1, v3
	v_permlane32_swap_b32_e32 v4, v6
	v_permlane32_swap_b32_e32 v5, v7
	v_permlane32_swap_b32_e32 v8, v10
	v_permlane32_swap_b32_e32 v9, v11
	v_permlane32_swap_b32_e32 v12, v14
	v_permlane32_swap_b32_e32 v13, v15
	ds_read_b64_tr_b16 v[162:163], v184 offset:0x8000
	ds_read_b64_tr_b16 v[164:165], v184 offset:0x8800
	ds_read_b64_tr_b16 v[166:167], v184 offset:0x9000
	ds_read_b64_tr_b16 v[168:169], v184 offset:0x9800
	ds_read_b64_tr_b16 v[170:171], v184 offset:0xa000
	ds_read_b64_tr_b16 v[172:173], v184 offset:0xa800
	ds_read_b64_tr_b16 v[174:175], v184 offset:0xb000
	ds_read_b64_tr_b16 v[176:177], v184 offset:0xb800
	s_waitcnt lgkmcnt(0)
	s_nop 0
	v_mfma_f32_32x32x16_f16 v[64:79], v[0:3], v[162:165], v[64:79]
	s_nop 2
	v_exp_f32_e32 v210, v112
	v_exp_f32_e32 v211, v113
	ds_read_b64_tr_b16 v[112:113], v184 offset:0x8200
	v_exp_f32_e32 v212, v114
	v_exp_f32_e32 v213, v115
	ds_read_b64_tr_b16 v[114:115], v184 offset:0x8a00
	ds_read_b64_tr_b16 v[162:163], v184 offset:0x9200
	v_mfma_f32_32x32x16_f16 v[64:79], v[4:7], v[166:169], v[64:79]
	ds_read_b64_tr_b16 v[164:165], v184 offset:0x9a00
	ds_read_b64_tr_b16 v[166:167], v184 offset:0xa200
	ds_read_b64_tr_b16 v[168:169], v184 offset:0xaa00
	v_mfma_f32_32x32x16_f16 v[64:79], v[8:11], v[170:173], v[64:79]
	ds_read_b64_tr_b16 v[170:171], v184 offset:0xb200
	ds_read_b64_tr_b16 v[172:173], v184 offset:0xba00
	v_mfma_f32_32x32x16_f16 v[64:79], v[12:15], v[174:177], v[64:79]
	s_waitcnt lgkmcnt(0)
	v_mfma_f32_32x32x16_f16 v[48:63], v[0:3], v[112:115], v[48:63]
	ds_read_b64_tr_b16 v[112:113], v184 offset:0x8400
	ds_read_b64_tr_b16 v[114:115], v184 offset:0x8c00
	v_exp_f32_e32 v214, v116
	v_exp_f32_e32 v215, v117
	ds_read_b64_tr_b16 v[116:117], v184 offset:0x9400
	v_exp_f32_e32 v216, v118
	v_exp_f32_e32 v217, v119
	v_mfma_f32_32x32x16_f16 v[48:63], v[4:7], v[162:165], v[48:63]
	ds_read_b64_tr_b16 v[118:119], v184 offset:0x9c00
	ds_read_b64_tr_b16 v[162:163], v184 offset:0xa400
	ds_read_b64_tr_b16 v[164:165], v184 offset:0xac00
	v_mfma_f32_32x32x16_f16 v[48:63], v[8:11], v[166:169], v[48:63]
	ds_read_b64_tr_b16 v[166:167], v184 offset:0xb400
	ds_read_b64_tr_b16 v[168:169], v184 offset:0xbc00
	v_mfma_f32_32x32x16_f16 v[48:63], v[12:15], v[170:173], v[48:63]
	s_waitcnt lgkmcnt(0)
	v_mfma_f32_32x32x16_f16 v[32:47], v[0:3], v[112:115], v[32:47]
	ds_read_b64_tr_b16 v[112:113], v184 offset:0x8600
	ds_read_b64_tr_b16 v[114:115], v184 offset:0x8e00
	v_exp_f32_e32 v218, v120
	v_exp_f32_e32 v219, v121
	v_exp_f32_e32 v220, v122
	v_exp_f32_e32 v221, v123
	v_mfma_f32_32x32x16_f16 v[32:47], v[4:7], v[116:119], v[32:47]
	ds_read_b64_tr_b16 v[116:117], v184 offset:0x9600
	ds_read_b64_tr_b16 v[118:119], v184 offset:0x9e00
	ds_read_b64_tr_b16 v[120:121], v184 offset:0xa600
	ds_read_b64_tr_b16 v[122:123], v184 offset:0xae00
	v_mfma_f32_32x32x16_f16 v[32:47], v[8:11], v[162:165], v[32:47]
	ds_read_b64_tr_b16 v[162:163], v184 offset:0xb600
	ds_read_b64_tr_b16 v[164:165], v184 offset:0xbe00
	v_mfma_f32_32x32x16_f16 v[32:47], v[12:15], v[166:169], v[32:47]
	s_waitcnt lgkmcnt(0)
	v_mfma_f32_32x32x16_f16 v[16:31], v[0:3], v[112:115], v[16:31]
	v_exp_f32_e32 v222, v124
	v_exp_f32_e32 v223, v125
	v_exp_f32_e32 v224, v126
	v_exp_f32_e32 v225, v127
	s_waitcnt vmcnt(0) lgkmcnt(0)
	s_barrier
	v_mfma_f32_32x32x16_f16 v[16:31], v[4:7], v[116:119], v[16:31]
	v_mfma_f32_32x32x16_f16 v[16:31], v[8:11], v[120:123], v[16:31]
	v_mfma_f32_32x32x16_f16 v[16:31], v[12:15], v[162:165], v[16:31]
	s_add_i32 s97, s97, 2
	s_add_i32 s1, s1, 4
	s_add_i32 s0, s0, 0x10000
	s_cmp_le_u32 s1, s99
	s_cbranch_scc1 .LBB3_3
	v_mul_i32_i24_e32 v0, -4, v160
	s_lshl_b32 s0, s4, 6
	v_subrev_u32_e32 v209, s0, v0
	s_cmp_gt_u32 s97, s99
	v_add_u32_e32 v160, v209, v161
	s_cbranch_scc1 .LBB3_18
	s_cmp_lt_u32 s97, s99
	s_cselect_b64 s[6:7], -1, 0
	s_cmp_ge_u32 s97, s99
	s_cselect_b64 s[4:5], -1, 0
	ds_read_b128 v[80:83], v190 offset:32768
	ds_read_b128 v[112:115], v190 offset:40960
	s_and_b64 vcc, exec, s[4:5]
	s_waitcnt lgkmcnt(1)
	v_mfma_f32_32x32x16_f16 v[0:15], v[80:83], v[156:159], -0.5
	s_waitcnt lgkmcnt(0)
	v_mfma_f32_32x32x16_f16 v[80:95], v[112:115], v[156:159], -0.5
	s_cbranch_vccnz .LBB3_7
	s_lshl_b32 s0, s97, 15
	s_add_i32 s0, s0, 0x8000
	s_mov_b32 m0, s86
	s_nop 0
	buffer_load_dwordx4 v191, s[68:71], s0 offen lds

.LBB3_17:
	v_add_f32_e32 v161, v161, v162
	ds_read_b64_tr_b16 v[162:163], v184 offset:0
	ds_read_b64_tr_b16 v[164:165], v184 offset:0x800
	ds_read_b64_tr_b16 v[166:167], v184 offset:0x1000
	ds_read_b64_tr_b16 v[168:169], v184 offset:0x1800
	ds_read_b64_tr_b16 v[170:171], v184 offset:0x2000
	ds_read_b64_tr_b16 v[172:173], v184 offset:0x2800
	ds_read_b64_tr_b16 v[174:175], v184 offset:0x3000
	ds_read_b64_tr_b16 v[176:177], v184 offset:0x3800
	s_waitcnt lgkmcnt(0)
	v_add_f32_e32 v185, v185, v161
	v_mfma_f32_32x32x16_f16 v[64:79], v[112:115], v[162:165], v[64:79]
	v_exp_f32_e32 v208, v0
	v_exp_f32_e32 v192, v1
	ds_read_b64_tr_b16 v[0:1], v184 offset:0x200
	v_exp_f32_e32 v193, v2
	v_exp_f32_e32 v194, v3
	ds_read_b64_tr_b16 v[2:3], v184 offset:0xa00
	ds_read_b64_tr_b16 v[162:163], v184 offset:0x1200
	v_mfma_f32_32x32x16_f16 v[64:79], v[120:123], v[166:169], v[64:79]
	ds_read_b64_tr_b16 v[164:165], v184 offset:0x1a00
	ds_read_b64_tr_b16 v[166:167], v184 offset:0x2200
	ds_read_b64_tr_b16 v[168:169], v184 offset:0x2a00
	v_mfma_f32_32x32x16_f16 v[64:79], v[124:127], v[170:173], v[64:79]
	ds_read_b64_tr_b16 v[170:171], v184 offset:0x3200
	ds_read_b64_tr_b16 v[172:173], v184 offset:0x3a00
	v_mfma_f32_32x32x16_f16 v[64:79], v[116:119], v[174:177], v[64:79]
	s_waitcnt lgkmcnt(0)
	v_mfma_f32_32x32x16_f16 v[48:63], v[112:115], v[0:3], v[48:63]
	ds_read_b64_tr_b16 v[0:1], v184 offset:0x400
	ds_read_b64_tr_b16 v[2:3], v184 offset:0xc00
	v_exp_f32_e32 v195, v4
	v_exp_f32_e32 v196, v5
	ds_read_b64_tr_b16 v[4:5], v184 offset:0x1400
	v_exp_f32_e32 v197, v6
	v_exp_f32_e32 v198, v7
	v_mfma_f32_32x32x16_f16 v[48:63], v[120:123], v[162:165], v[48:63]
	ds_read_b64_tr_b16 v[6:7], v184 offset:0x1c00
	ds_read_b64_tr_b16 v[162:163], v184 offset:0x2400
	ds_read_b64_tr_b16 v[164:165], v184 offset:0x2c00
	v_mfma_f32_32x32x16_f16 v[48:63], v[124:127], v[166:169], v[48:63]
	ds_read_b64_tr_b16 v[166:167], v184 offset:0x3400
	ds_read_b64_tr_b16 v[168:169], v184 offset:0x3c00
	v_mfma_f32_32x32x16_f16 v[48:63], v[116:119], v[170:173], v[48:63]
	s_waitcnt lgkmcnt(0)
	v_mfma_f32_32x32x16_f16 v[32:47], v[112:115], v[0:3], v[32:47]
	ds_read_b64_tr_b16 v[0:1], v184 offset:0x600
	ds_read_b64_tr_b16 v[2:3], v184 offset:0xe00
	v_exp_f32_e32 v199, v8
	v_exp_f32_e32 v200, v9
	v_exp_f32_e32 v201, v10
	v_exp_f32_e32 v202, v11
	v_mfma_f32_32x32x16_f16 v[32:47], v[120:123], v[4:7], v[32:47]
	ds_read_b64_tr_b16 v[4:5], v184 offset:0x1600
	ds_read_b64_tr_b16 v[6:7], v184 offset:0x1e00
	ds_read_b64_tr_b16 v[8:9], v184 offset:0x2600
	ds_read_b64_tr_b16 v[10:11], v184 offset:0x2e00
	v_mfma_f32_32x32x16_f16 v[32:47], v[124:127], v[162:165], v[32:47]
	ds_read_b64_tr_b16 v[162:163], v184 offset:0x3600
	ds_read_b64_tr_b16 v[164:165], v184 offset:0x3e00
	v_mfma_f32_32x32x16_f16 v[32:47], v[116:119], v[166:169], v[32:47]
	s_waitcnt lgkmcnt(0)
	v_mfma_f32_32x32x16_f16 v[16:31], v[112:115], v[0:3], v[16:31]
	v_exp_f32_e32 v203, v12
	v_exp_f32_e32 v204, v13
	v_exp_f32_e32 v205, v14
	v_exp_f32_e32 v206, v15
	s_waitcnt vmcnt(0) lgkmcnt(0)
	s_barrier
	v_mfma_f32_32x32x16_f16 v[16:31], v[120:123], v[4:7], v[16:31]
	v_mfma_f32_32x32x16_f16 v[16:31], v[124:127], v[8:11], v[16:31]
	v_mfma_f32_32x32x16_f16 v[16:31], v[116:119], v[162:165], v[16:31]
.LBB3_18:
	s_cmp_ge_u32 s97, s99
	v_cvt_pk_f16_f32 v180, v208, v192
	v_cvt_pk_f16_f32 v181, v193, v194
	v_cvt_pk_f16_f32 v182, v195, v196
	v_cvt_pk_f16_f32 v183, v197, v198
	v_cvt_pk_f16_f32 v176, v199, v200
	v_cvt_pk_f16_f32 v177, v201, v202
	v_cvt_pk_f16_f32 v178, v203, v204
	v_cvt_pk_f16_f32 v179, v205, v206
	v_add_f32_e32 v161, 0, v208
	s_cbranch_scc1 .LBB3_20
	ds_read_b128 v[0:3], v189
	ds_read_b128 v[4:7], v190
	ds_read_b128 v[112:115], v189 offset:8192
	ds_read_b128 v[116:119], v190 offset:128
	ds_read_b128 v[120:123], v190 offset:8192
	ds_read_b128 v[124:127], v190 offset:8320
	s_lshl_b32 s0, s97, 15
	s_waitcnt lgkmcnt(4)
	v_mfma_f32_32x32x16_f16 v[96:111], v[4:7], v[156:159], -0.5
	s_mov_b32 m0, s3
	v_mfma_f32_32x32x16_f16 v[96:111], v[0:3], v[152:155], v[96:111]
	s_waitcnt lgkmcnt(1)
	v_mfma_f32_32x32x16_f16 v[0:15], v[120:123], v[156:159], -0.5
	ds_read_b128 v[120:123], v188 offset:8192
	ds_read_b128 v[156:159], v188
	s_add_i32 s1, s0, 0x8000
	s_mov_b32 s74, s70
	s_mov_b32 s75, s71
	v_exp_f32_e32 v80, v80
	v_exp_f32_e32 v81, v81
	v_mfma_f32_32x32x16_f16 v[0:15], v[112:115], v[152:155], v[0:15]
	ds_read_b128 v[112:115], v187 offset:8192
	ds_read_b128 v[152:155], v187
	buffer_load_dwordx4 v186, s[72:75], s1 offen lds
	s_add_i32 s1, s0, 0xa000
	s_mov_b32 m0, s82
	v_exp_f32_e32 v82, v82
	v_exp_f32_e32 v83, v83
	v_exp_f32_e32 v84, v84
	s_waitcnt lgkmcnt(2)
	v_mfma_f32_32x32x16_f16 v[96:111], v[156:159], v[148:151], v[96:111]
	ds_read_b128 v[156:159], v189 offset:8320
	ds_read_b128 v[162:165], v189 offset:128
	buffer_load_dwordx4 v186, s[72:75], s1 offen lds
	s_add_i32 s1, s0, 0xc000
	s_mov_b32 m0, s81
	ds_read_b128 v[166:169], v188 offset:8320
	ds_read_b128 v[170:173], v188 offset:128
	buffer_load_dwordx4 v186, s[72:75], s1 offen lds
	s_add_i32 s0, s0, 0xe000
	s_mov_b32 m0, s80
	v_mfma_f32_32x32x16_f16 v[0:15], v[120:123], v[148:151], v[0:15]
	ds_read_b128 v[120:123], v187 offset:8320
	ds_read_b128 v[148:151], v187 offset:128
	buffer_load_dwordx4 v186, s[72:75], s0 offen lds
	v_exp_f32_e32 v85, v85
	v_exp_f32_e32 v86, v86
	v_exp_f32_e32 v87, v87
	v_exp_f32_e32 v88, v88
	v_exp_f32_e32 v89, v89
	s_waitcnt lgkmcnt(6)
	v_mfma_f32_32x32x16_f16 v[96:111], v[152:155], v[144:147], v[96:111]
	v_exp_f32_e32 v90, v90
	v_exp_f32_e32 v91, v91
	v_exp_f32_e32 v92, v92
	v_exp_f32_e32 v93, v93
	v_exp_f32_e32 v94, v94
	v_exp_f32_e32 v95, v95
	v_mfma_f32_32x32x16_f16 v[0:15], v[112:115], v[144:147], v[0:15]
	v_add_f32_e32 v112, v192, v161
	v_add_f32_e32 v112, v193, v112
	v_add_f32_e32 v112, v194, v112
	v_add_f32_e32 v112, v195, v112
	v_add_f32_e32 v112, v196, v112
	v_add_f32_e32 v112, v197, v112
	v_add_f32_e32 v112, v198, v112
	v_mfma_f32_32x32x16_f16 v[96:111], v[116:119], v[140:143], v[96:111]
	v_add_f32_e32 v112, v199, v112
	v_add_f32_e32 v112, v200, v112
	v_add_f32_e32 v112, v201, v112
	v_add_f32_e32 v112, v202, v112
	v_add_f32_e32 v112, v203, v112
	v_add_f32_e32 v112, v204, v112
	v_add_f32_e32 v112, v205, v112
	v_mfma_f32_32x32x16_f16 v[0:15], v[124:127], v[140:143], v[0:15]
	v_add_f32_e32 v112, v206, v112
	v_add_f32_e32 v112, v80, v112
	v_add_f32_e32 v112, v81, v112
	v_add_f32_e32 v112, v82, v112
	v_add_f32_e32 v112, v83, v112
	v_add_f32_e32 v112, v84, v112
	v_add_f32_e32 v112, v85, v112
	s_waitcnt lgkmcnt(4)
	v_mfma_f32_32x32x16_f16 v[96:111], v[162:165], v[136:139], v[96:111]
	v_add_f32_e32 v112, v86, v112
	v_add_f32_e32 v112, v87, v112
	v_add_f32_e32 v112, v88, v112
	v_add_f32_e32 v112, v89, v112
	v_add_f32_e32 v112, v90, v112
	v_add_f32_e32 v112, v91, v112
	v_add_f32_e32 v112, v92, v112
	v_mfma_f32_32x32x16_f16 v[0:15], v[156:159], v[136:139], v[0:15]
	v_add_f32_e32 v112, v93, v112
	v_add_f32_e32 v112, v94, v112
	v_add_f32_e32 v112, v95, v112
	v_mov_b32_e32 v113, v112
	s_nop 1
	v_permlane32_swap_b32_e32 v112, v113
	v_add_f32_e32 v112, v112, v113
	s_waitcnt lgkmcnt(2)
	v_mfma_f32_32x32x16_f16 v[96:111], v[170:173], v[132:135], v[96:111]
	v_add_f32_e32 v185, v185, v112
	v_mov_b32_e32 v112, v180
	v_mov_b32_e32 v114, v182
	v_mov_b32_e32 v113, v181
	v_mov_b32_e32 v115, v183
	v_mov_b32_e32 v116, v176
	v_mov_b32_e32 v118, v178
	v_mfma_f32_32x32x16_f16 v[0:15], v[166:169], v[132:135], v[0:15]
	v_mov_b32_e32 v117, v177
	v_mov_b32_e32 v119, v179
	v_cvt_pk_f16_f32 v124, v80, v81
	v_cvt_pk_f16_f32 v125, v82, v83
	v_cvt_pk_f16_f32 v126, v84, v85
	v_cvt_pk_f16_f32 v127, v86, v87
	v_permlane32_swap_b32_e32 v112, v114
	s_waitcnt lgkmcnt(0)
	v_mfma_f32_32x32x16_f16 v[96:111], v[148:151], v[128:131], v[96:111]
	v_permlane32_swap_b32_e32 v113, v115
	v_permlane32_swap_b32_e32 v116, v118
	v_permlane32_swap_b32_e32 v117, v119
	v_permlane32_swap_b32_e32 v124, v126
	v_mfma_f32_32x32x16_f16 v[0:15], v[120:123], v[128:131], v[0:15]
	v_cvt_pk_f16_f32 v120, v88, v89
	v_cvt_pk_f16_f32 v121, v90, v91
	v_cvt_pk_f16_f32 v122, v92, v93
	v_cvt_pk_f16_f32 v123, v94, v95
	v_permlane32_swap_b32_e32 v125, v127
	v_permlane32_swap_b32_e32 v120, v122
	v_permlane32_swap_b32_e32 v121, v123
	s_lshl_b32 s0, s97, 7
	v_subrev_u32_e32 v128, s0, v160
	v_add_u32_e32 v128, 0xffffff80, v128
	v_mov_b32_e32 v129, 0xff800000
	v_cmp_gt_i32_e64 s[58:59], 26, v128
	v_cmp_gt_i32_e64 s[62:63], 27, v128
	v_cmp_gt_i32_e64 s[56:57], 25, v128
	s_and_b64 s[58:59], s[62:63], s[58:59]
	v_cmp_gt_i32_e64 s[54:55], 24, v128
	s_and_b64 s[56:57], s[58:59], s[56:57]
	v_cmp_gt_i32_e64 s[52:53], 19, v128
	s_and_b64 s[54:55], s[56:57], s[54:55]
	v_cmp_gt_i32_e64 s[50:51], 18, v128
	s_and_b64 s[52:53], s[54:55], s[52:53]
	v_cmp_gt_i32_e64 s[48:49], 17, v128
	s_and_b64 s[50:51], s[52:53], s[50:51]
	v_cmp_gt_i32_e64 s[46:47], 16, v128
	s_and_b64 s[48:49], s[50:51], s[48:49]
	v_cmp_gt_i32_e64 s[44:45], 11, v128
	s_and_b64 s[46:47], s[48:49], s[46:47]
	v_cmp_gt_i32_e64 s[42:43], 10, v128
	s_and_b64 s[44:45], s[46:47], s[44:45]
	v_cmp_gt_i32_e64 s[40:41], 9, v128
	s_and_b64 s[42:43], s[44:45], s[42:43]
	v_cmp_gt_i32_e64 s[38:39], 8, v128
	s_and_b64 s[40:41], s[42:43], s[40:41]
	v_cmp_gt_i32_e64 s[36:37], 3, v128
	s_and_b64 s[38:39], s[40:41], s[38:39]
	v_cmp_gt_i32_e64 s[34:35], 2, v128
	s_and_b64 s[36:37], s[38:39], s[36:37]
	v_cmp_gt_i32_e64 s[30:31], 1, v128
	s_and_b64 s[34:35], s[36:37], s[34:35]
	v_cmp_gt_i32_e64 s[28:29], 0, v128
	s_and_b64 s[30:31], s[34:35], s[30:31]
	s_and_b64 s[28:29], s[30:31], s[28:29]
	v_cmp_gt_i32_e64 s[60:61], 58, v128
	v_cndmask_b32_e64 v145, v96, v129, s[28:29]
	v_cmp_gt_i32_e64 s[28:29], 59, v128
	v_cmp_gt_i32_e64 s[24:25], 57, v128
	v_cndmask_b32_e64 v132, v111, v129, s[62:63]
	v_cndmask_b32_e64 v111, v15, v129, s[28:29]
	s_and_b64 s[28:29], s[28:29], s[60:61]
	v_cmp_gt_i32_e64 s[22:23], 56, v128
	s_and_b64 s[24:25], s[28:29], s[24:25]
	v_cmp_gt_i32_e64 s[20:21], 51, v128
	s_and_b64 s[22:23], s[24:25], s[22:23]
	v_cmp_gt_i32_e64 s[18:19], 50, v128
	s_and_b64 s[20:21], s[22:23], s[20:21]
	v_cmp_gt_i32_e64 s[16:17], 49, v128
	s_and_b64 s[18:19], s[20:21], s[18:19]
	v_cmp_gt_i32_e64 s[14:15], 48, v128
	s_and_b64 s[16:17], s[18:19], s[16:17]
	v_cmp_gt_i32_e64 s[12:13], 43, v128
	s_and_b64 s[14:15], s[16:17], s[14:15]
	v_cmp_gt_i32_e64 s[10:11], 42, v128
	s_and_b64 s[12:13], s[14:15], s[12:13]
	v_cmp_gt_i32_e64 s[8:9], 41, v128
	s_and_b64 s[10:11], s[12:13], s[10:11]
	v_cmp_gt_i32_e64 s[6:7], 40, v128
	s_and_b64 s[8:9], s[10:11], s[8:9]
	v_cmp_gt_i32_e64 s[4:5], 35, v128
	s_and_b64 s[6:7], s[8:9], s[6:7]
	v_cmp_gt_i32_e64 s[26:27], 34, v128
	s_and_b64 s[4:5], s[6:7], s[4:5]
	v_cmp_gt_i32_e64 s[0:1], 33, v128
	v_cndmask_b32_e64 v130, v99, v129, s[36:37]
	v_cndmask_b32_e64 v99, v3, v129, s[4:5]
	s_and_b64 s[4:5], s[4:5], s[26:27]
	v_cmp_gt_i32_e32 vcc, 32, v128
	s_and_b64 s[0:1], s[4:5], s[0:1]
	s_and_b64 vcc, s[0:1], vcc
	v_cndmask_b32_e64 v144, v97, v129, s[30:31]
	v_cndmask_b32_e64 v97, v1, v129, s[0:1]
	v_cndmask_b32_e32 v96, v0, v129, vcc
	ds_read_b64_tr_b16 v[0:1], v184 offset:0x8000
	v_cndmask_b32_e64 v131, v98, v129, s[34:35]
	v_cndmask_b32_e64 v98, v2, v129, s[4:5]
	ds_read_b64_tr_b16 v[2:3], v184 offset:0x8800
	v_cndmask_b32_e64 v142, v101, v129, s[40:41]
	v_cndmask_b32_e64 v143, v100, v129, s[38:39]
	v_cndmask_b32_e64 v101, v5, v129, s[8:9]
	v_cndmask_b32_e64 v100, v4, v129, s[6:7]
	ds_read_b64_tr_b16 v[4:5], v184 offset:0x9000
	v_cndmask_b32_e64 v140, v103, v129, s[44:45]
	v_cndmask_b32_e64 v141, v102, v129, s[42:43]
	v_cndmask_b32_e64 v103, v7, v129, s[12:13]
	v_cndmask_b32_e64 v102, v6, v129, s[10:11]
	ds_read_b64_tr_b16 v[6:7], v184 offset:0x9800
	v_cndmask_b32_e64 v138, v105, v129, s[48:49]
	v_cndmask_b32_e64 v139, v104, v129, s[46:47]
	v_cndmask_b32_e64 v105, v9, v129, s[16:17]
	v_cndmask_b32_e64 v104, v8, v129, s[14:15]
	ds_read_b64_tr_b16 v[8:9], v184 offset:0xa000
	v_cndmask_b32_e64 v136, v107, v129, s[52:53]
	v_cndmask_b32_e64 v137, v106, v129, s[50:51]
	v_cndmask_b32_e64 v107, v11, v129, s[20:21]
	v_cndmask_b32_e64 v106, v10, v129, s[18:19]
	ds_read_b64_tr_b16 v[10:11], v184 offset:0xa800
	v_cndmask_b32_e64 v134, v109, v129, s[56:57]
	v_cndmask_b32_e64 v135, v108, v129, s[54:55]
	v_cndmask_b32_e64 v109, v13, v129, s[24:25]
	v_cndmask_b32_e64 v108, v12, v129, s[22:23]
	ds_read_b64_tr_b16 v[12:13], v184 offset:0xb000
	v_cndmask_b32_e64 v133, v110, v129, s[58:59]
	v_cndmask_b32_e64 v110, v14, v129, s[28:29]
	ds_read_b64_tr_b16 v[14:15], v184 offset:0xb800
	s_waitcnt lgkmcnt(0)
	v_mfma_f32_32x32x16_f16 v[64:79], v[112:115], v[0:3], v[64:79]
	ds_read_b64_tr_b16 v[0:1], v184 offset:0x8200
	ds_read_b64_tr_b16 v[2:3], v184 offset:0x8a00
	v_exp_f32_e32 v210, v145
	v_exp_f32_e32 v211, v144
	v_exp_f32_e32 v212, v131
	v_exp_f32_e32 v213, v130
	v_mfma_f32_32x32x16_f16 v[64:79], v[116:119], v[4:7], v[64:79]
	ds_read_b64_tr_b16 v[4:5], v184 offset:0x9200
	ds_read_b64_tr_b16 v[6:7], v184 offset:0x9a00
	v_mfma_f32_32x32x16_f16 v[64:79], v[124:127], v[8:11], v[64:79]
	ds_read_b64_tr_b16 v[8:9], v184 offset:0xa200
	ds_read_b64_tr_b16 v[10:11], v184 offset:0xaa00
	ds_read_b64_tr_b16 v[128:129], v184 offset:0xb200
	ds_read_b64_tr_b16 v[130:131], v184 offset:0xba00
	v_mfma_f32_32x32x16_f16 v[64:79], v[120:123], v[12:15], v[64:79]
	s_waitcnt lgkmcnt(0)
	v_mfma_f32_32x32x16_f16 v[48:63], v[112:115], v[0:3], v[48:63]
	ds_read_b64_tr_b16 v[0:1], v184 offset:0x8400
	ds_read_b64_tr_b16 v[2:3], v184 offset:0x8c00
	v_exp_f32_e32 v214, v143
	v_exp_f32_e32 v215, v142
	v_exp_f32_e32 v216, v141
	v_exp_f32_e32 v217, v140
	v_mfma_f32_32x32x16_f16 v[48:63], v[116:119], v[4:7], v[48:63]
	ds_read_b64_tr_b16 v[4:5], v184 offset:0x9400
	ds_read_b64_tr_b16 v[6:7], v184 offset:0x9c00
	v_mfma_f32_32x32x16_f16 v[48:63], v[124:127], v[8:11], v[48:63]
	ds_read_b64_tr_b16 v[8:9], v184 offset:0xa400
	ds_read_b64_tr_b16 v[10:11], v184 offset:0xac00
	ds_read_b64_tr_b16 v[12:13], v184 offset:0xb400
	ds_read_b64_tr_b16 v[14:15], v184 offset:0xbc00
	v_mfma_f32_32x32x16_f16 v[48:63], v[120:123], v[128:131], v[48:63]
	s_waitcnt lgkmcnt(0)
	v_mfma_f32_32x32x16_f16 v[32:47], v[112:115], v[0:3], v[32:47]
	ds_read_b64_tr_b16 v[0:1], v184 offset:0x8600
	ds_read_b64_tr_b16 v[2:3], v184 offset:0x8e00
	v_exp_f32_e32 v218, v139
	v_exp_f32_e32 v219, v138
	v_exp_f32_e32 v220, v137
	v_exp_f32_e32 v221, v136
	v_mfma_f32_32x32x16_f16 v[32:47], v[116:119], v[4:7], v[32:47]
	ds_read_b64_tr_b16 v[4:5], v184 offset:0x9600
	ds_read_b64_tr_b16 v[6:7], v184 offset:0x9e00
	v_mfma_f32_32x32x16_f16 v[32:47], v[124:127], v[8:11], v[32:47]
	ds_read_b64_tr_b16 v[8:9], v184 offset:0xa600
	ds_read_b64_tr_b16 v[10:11], v184 offset:0xae00
	ds_read_b64_tr_b16 v[128:129], v184 offset:0xb600
	ds_read_b64_tr_b16 v[130:131], v184 offset:0xbe00
	v_mfma_f32_32x32x16_f16 v[32:47], v[120:123], v[12:15], v[32:47]
	s_waitcnt lgkmcnt(0)
	v_mfma_f32_32x32x16_f16 v[16:31], v[112:115], v[0:3], v[16:31]
	v_exp_f32_e32 v222, v135
	v_exp_f32_e32 v223, v134
	v_exp_f32_e32 v224, v133
	v_exp_f32_e32 v225, v132
	s_waitcnt vmcnt(0) lgkmcnt(0)
	s_barrier
	v_mfma_f32_32x32x16_f16 v[16:31], v[116:119], v[4:7], v[16:31]
	v_mfma_f32_32x32x16_f16 v[16:31], v[124:127], v[8:11], v[16:31]
	v_mfma_f32_32x32x16_f16 v[16:31], v[120:123], v[128:131], v[16:31]
.LBB3_20:
	s_bitcmp0_b32 s99, 0
	s_cbranch_scc1 .LBB3_22
	v_add_f32_e32 v112, v192, v161
	v_add_f32_e32 v112, v193, v112
	v_add_f32_e32 v112, v194, v112
	v_add_f32_e32 v112, v195, v112
	v_add_f32_e32 v112, v196, v112
	v_add_f32_e32 v112, v197, v112
	v_add_f32_e32 v112, v198, v112
	v_add_f32_e32 v112, v199, v112
	v_add_f32_e32 v112, v200, v112
	v_add_f32_e32 v112, v201, v112
	v_add_f32_e32 v112, v202, v112
	v_exp_f32_e32 v0, v80
	v_add_f32_e32 v112, v203, v112
	v_exp_f32_e32 v1, v81
	v_add_f32_e32 v112, v204, v112
	v_exp_f32_e32 v2, v82
	v_add_f32_e32 v112, v205, v112
	v_exp_f32_e32 v3, v83
	v_add_f32_e32 v112, v206, v112
	v_exp_f32_e32 v4, v84
	v_add_f32_e32 v112, v112, v0
	v_exp_f32_e32 v5, v85
	v_add_f32_e32 v112, v1, v112
	v_exp_f32_e32 v6, v86
	v_add_f32_e32 v112, v2, v112
	v_exp_f32_e32 v7, v87
	v_add_f32_e32 v112, v3, v112
	v_exp_f32_e32 v8, v88
	v_add_f32_e32 v112, v4, v112
	v_exp_f32_e32 v9, v89
	v_add_f32_e32 v112, v5, v112
	v_exp_f32_e32 v10, v90
	v_add_f32_e32 v112, v6, v112
	v_exp_f32_e32 v11, v91
	v_add_f32_e32 v112, v7, v112
	v_exp_f32_e32 v12, v92
	v_add_f32_e32 v112, v8, v112
	v_exp_f32_e32 v13, v93
	v_add_f32_e32 v112, v9, v112
	v_exp_f32_e32 v14, v94
	v_add_f32_e32 v112, v10, v112
	v_exp_f32_e32 v15, v95
	v_add_f32_e32 v112, v11, v112
	v_add_f32_e32 v112, v12, v112
	v_add_f32_e32 v112, v13, v112
	v_add_f32_e32 v112, v14, v112
	v_add_f32_e32 v112, v15, v112
	v_mov_b32_e32 v113, v112
	s_nop 1
	v_permlane32_swap_b32_e32 v112, v113
	v_add_f32_e32 v226, v112, v113
	v_cvt_pk_f16_f32 v228, v0, v1
	v_cvt_pk_f16_f32 v229, v2, v3
	v_cvt_pk_f16_f32 v230, v4, v5
	v_cvt_pk_f16_f32 v231, v6, v7
	v_cvt_pk_f16_f32 v232, v8, v9
	v_cvt_pk_f16_f32 v233, v10, v11
	v_cvt_pk_f16_f32 v234, v12, v13
	v_cvt_pk_f16_f32 v235, v14, v15
	v_permlane32_swap_b32_e32 v180, v182
	v_permlane32_swap_b32_e32 v181, v183
	v_permlane32_swap_b32_e32 v176, v178
	v_permlane32_swap_b32_e32 v177, v179
	v_permlane32_swap_b32_e32 v228, v230
	v_permlane32_swap_b32_e32 v229, v231
	v_permlane32_swap_b32_e32 v232, v234
	v_permlane32_swap_b32_e32 v233, v235
	ds_read_b64_tr_b16 v[128:129], v184 offset:0x8000
	ds_read_b64_tr_b16 v[130:131], v184 offset:0x8800
	ds_read_b64_tr_b16 v[132:133], v184 offset:0x9000
	ds_read_b64_tr_b16 v[134:135], v184 offset:0x9800
	ds_read_b64_tr_b16 v[136:137], v184 offset:0xa000
	ds_read_b64_tr_b16 v[138:139], v184 offset:0xa800
	ds_read_b64_tr_b16 v[140:141], v184 offset:0xb000
	ds_read_b64_tr_b16 v[142:143], v184 offset:0xb800
	s_waitcnt lgkmcnt(0)
	s_nop 0
	v_mfma_f32_32x32x16_f16 v[112:127], v[180:183], v[128:131], v[64:79]
	ds_read_b64_tr_b16 v[144:145], v184 offset:0x8200
	ds_read_b64_tr_b16 v[146:147], v184 offset:0x8a00
	ds_read_b64_tr_b16 v[148:149], v184 offset:0x9200
	ds_read_b64_tr_b16 v[150:151], v184 offset:0x9a00
	ds_read_b64_tr_b16 v[152:153], v184 offset:0xa200
	ds_read_b64_tr_b16 v[154:155], v184 offset:0xaa00
	ds_read_b64_tr_b16 v[156:157], v184 offset:0xb200
	v_mfma_f32_32x32x16_f16 v[112:127], v[176:179], v[132:135], v[112:127]
	ds_read_b64_tr_b16 v[158:159], v184 offset:0xba00
	v_mfma_f32_32x32x16_f16 v[112:127], v[228:231], v[136:139], v[112:127]
	v_mfma_f32_32x32x16_f16 v[112:127], v[232:235], v[140:143], v[112:127]
	s_waitcnt lgkmcnt(0)
	v_mfma_f32_32x32x16_f16 v[128:143], v[180:183], v[144:147], v[48:63]
	ds_read_b64_tr_b16 v[160:161], v184 offset:0x8400
	ds_read_b64_tr_b16 v[162:163], v184 offset:0x8c00
	ds_read_b64_tr_b16 v[164:165], v184 offset:0x9400
	ds_read_b64_tr_b16 v[166:167], v184 offset:0x9c00
	ds_read_b64_tr_b16 v[168:169], v184 offset:0xa400
	ds_read_b64_tr_b16 v[170:171], v184 offset:0xac00
	ds_read_b64_tr_b16 v[172:173], v184 offset:0xb400
	v_mfma_f32_32x32x16_f16 v[128:143], v[176:179], v[148:151], v[128:143]
	ds_read_b64_tr_b16 v[174:175], v184 offset:0xbc00
	v_mfma_f32_32x32x16_f16 v[128:143], v[228:231], v[152:155], v[128:143]
	v_mfma_f32_32x32x16_f16 v[128:143], v[232:235], v[156:159], v[128:143]
	s_waitcnt lgkmcnt(0)
	v_mfma_f32_32x32x16_f16 v[144:159], v[180:183], v[160:163], v[32:47]
	ds_read_b64_tr_b16 v[236:237], v184 offset:0x8600
	ds_read_b64_tr_b16 v[238:239], v184 offset:0x8e00
	ds_read_b64_tr_b16 v[240:241], v184 offset:0x9600
	ds_read_b64_tr_b16 v[242:243], v184 offset:0x9e00
	ds_read_b64_tr_b16 v[244:245], v184 offset:0xa600
	ds_read_b64_tr_b16 v[246:247], v184 offset:0xae00
	ds_read_b64_tr_b16 v[248:249], v184 offset:0xb600
	v_mfma_f32_32x32x16_f16 v[144:159], v[176:179], v[164:167], v[144:159]
	ds_read_b64_tr_b16 v[250:251], v184 offset:0xbe00
	v_mfma_f32_32x32x16_f16 v[144:159], v[228:231], v[168:171], v[144:159]
	v_mfma_f32_32x32x16_f16 v[144:159], v[232:235], v[172:175], v[144:159]
	s_waitcnt lgkmcnt(0)
	v_mfma_f32_32x32x16_f16 v[160:175], v[180:183], v[236:239], v[16:31]
	v_mfma_f32_32x32x16_f16 v[160:175], v[176:179], v[240:243], v[160:175]
	v_mfma_f32_32x32x16_f16 v[160:175], v[228:231], v[244:247], v[160:175]
	v_mfma_f32_32x32x16_f16 v[160:175], v[232:235], v[248:251], v[160:175]
	s_cbranch_execz .LBB3_23
	s_branch .LBB3_24
.LBB3_22:
.LBB3_23:
	v_add_f32_e32 v0, 0, v210
	v_add_f32_e32 v0, v211, v0
	v_add_f32_e32 v0, v212, v0
	v_add_f32_e32 v0, v213, v0
	v_add_f32_e32 v0, v214, v0
	v_add_f32_e32 v0, v215, v0
	v_add_f32_e32 v0, v216, v0
	v_add_f32_e32 v0, v217, v0
	v_add_f32_e32 v0, v218, v0
	v_add_f32_e32 v0, v219, v0
	v_add_f32_e32 v0, v220, v0
	v_add_f32_e32 v0, v221, v0
	v_exp_f32_e32 v8, v96
	v_add_f32_e32 v0, v222, v0
	v_exp_f32_e32 v9, v97
	v_add_f32_e32 v0, v223, v0
	v_exp_f32_e32 v10, v98
	v_add_f32_e32 v0, v224, v0
	v_exp_f32_e32 v11, v99
	v_add_f32_e32 v0, v225, v0
	v_exp_f32_e32 v12, v100
	v_add_f32_e32 v0, v8, v0
	v_exp_f32_e32 v13, v101
	v_add_f32_e32 v0, v9, v0
	v_exp_f32_e32 v14, v102
	v_add_f32_e32 v0, v10, v0
	v_exp_f32_e32 v15, v103
	v_add_f32_e32 v0, v11, v0
	v_exp_f32_e32 v96, v104
	v_add_f32_e32 v0, v12, v0
	v_exp_f32_e32 v97, v105
	v_add_f32_e32 v0, v13, v0
	v_exp_f32_e32 v98, v106
	v_add_f32_e32 v0, v14, v0
	v_exp_f32_e32 v99, v107
	v_add_f32_e32 v0, v15, v0
	v_exp_f32_e32 v100, v108
	v_add_f32_e32 v0, v96, v0
	v_exp_f32_e32 v101, v109
	v_add_f32_e32 v0, v97, v0
	v_exp_f32_e32 v102, v110
	v_add_f32_e32 v0, v98, v0
	v_exp_f32_e32 v103, v111
	v_add_f32_e32 v0, v99, v0
	v_add_f32_e32 v0, v100, v0
	v_add_f32_e32 v0, v101, v0
	v_add_f32_e32 v0, v102, v0
	v_add_f32_e32 v0, v103, v0
	v_mov_b32_e32 v1, v0
	s_nop 1
	v_permlane32_swap_b32_e32 v0, v1
	v_add_f32_e32 v226, v0, v1
	v_cvt_pk_f16_f32 v0, v210, v211
	v_cvt_pk_f16_f32 v1, v212, v213
	v_cvt_pk_f16_f32 v2, v214, v215
	v_cvt_pk_f16_f32 v3, v216, v217
	v_cvt_pk_f16_f32 v4, v218, v219
	v_cvt_pk_f16_f32 v5, v220, v221
	v_cvt_pk_f16_f32 v6, v222, v223
	v_cvt_pk_f16_f32 v7, v224, v225
	v_cvt_pk_f16_f32 v8, v8, v9
	v_cvt_pk_f16_f32 v9, v10, v11
	v_cvt_pk_f16_f32 v10, v12, v13
	v_cvt_pk_f16_f32 v11, v14, v15
	v_cvt_pk_f16_f32 v12, v96, v97
	v_cvt_pk_f16_f32 v13, v98, v99
	v_cvt_pk_f16_f32 v14, v100, v101
	v_cvt_pk_f16_f32 v15, v102, v103
	v_permlane32_swap_b32_e32 v0, v2
	v_permlane32_swap_b32_e32 v1, v3
	v_permlane32_swap_b32_e32 v4, v6
	v_permlane32_swap_b32_e32 v5, v7
	v_permlane32_swap_b32_e32 v8, v10
	v_permlane32_swap_b32_e32 v9, v11
	v_permlane32_swap_b32_e32 v12, v14
	v_permlane32_swap_b32_e32 v13, v15
	ds_read_b64_tr_b16 v[96:97], v184 offset:0
	ds_read_b64_tr_b16 v[98:99], v184 offset:0x800
	ds_read_b64_tr_b16 v[100:101], v184 offset:0x1000
	ds_read_b64_tr_b16 v[102:103], v184 offset:0x1800
	ds_read_b64_tr_b16 v[104:105], v184 offset:0x2000
	ds_read_b64_tr_b16 v[106:107], v184 offset:0x2800
	ds_read_b64_tr_b16 v[108:109], v184 offset:0x3000
	ds_read_b64_tr_b16 v[110:111], v184 offset:0x3800
	s_waitcnt lgkmcnt(0)
	s_nop 0
	v_mfma_f32_32x32x16_f16 v[64:79], v[0:3], v[96:99], v[64:79]
	ds_read_b64_tr_b16 v[96:97], v184 offset:0x200
	ds_read_b64_tr_b16 v[98:99], v184 offset:0xa00
	v_mfma_f32_32x32x16_f16 v[64:79], v[4:7], v[100:103], v[64:79]
	ds_read_b64_tr_b16 v[100:101], v184 offset:0x1200
	ds_read_b64_tr_b16 v[102:103], v184 offset:0x1a00
	v_mfma_f32_32x32x16_f16 v[64:79], v[8:11], v[104:107], v[64:79]
	ds_read_b64_tr_b16 v[104:105], v184 offset:0x2200
	ds_read_b64_tr_b16 v[106:107], v184 offset:0x2a00
	ds_read_b64_tr_b16 v[112:113], v184 offset:0x3200
	ds_read_b64_tr_b16 v[114:115], v184 offset:0x3a00
	v_mfma_f32_32x32x16_f16 v[64:79], v[12:15], v[108:111], v[64:79]
	s_waitcnt lgkmcnt(0)
	v_mfma_f32_32x32x16_f16 v[48:63], v[0:3], v[96:99], v[48:63]
	ds_read_b64_tr_b16 v[96:97], v184 offset:0x400
	ds_read_b64_tr_b16 v[98:99], v184 offset:0xc00
	v_mfma_f32_32x32x16_f16 v[48:63], v[4:7], v[100:103], v[48:63]
	ds_read_b64_tr_b16 v[100:101], v184 offset:0x1400
	ds_read_b64_tr_b16 v[102:103], v184 offset:0x1c00
	v_mfma_f32_32x32x16_f16 v[48:63], v[8:11], v[104:107], v[48:63]
	ds_read_b64_tr_b16 v[104:105], v184 offset:0x2400
	ds_read_b64_tr_b16 v[106:107], v184 offset:0x2c00
	ds_read_b64_tr_b16 v[108:109], v184 offset:0x3400
	ds_read_b64_tr_b16 v[110:111], v184 offset:0x3c00
	v_mfma_f32_32x32x16_f16 v[48:63], v[12:15], v[112:115], v[48:63]
	s_waitcnt lgkmcnt(0)
	v_mfma_f32_32x32x16_f16 v[32:47], v[0:3], v[96:99], v[32:47]
	ds_read_b64_tr_b16 v[96:97], v184 offset:0x600
	ds_read_b64_tr_b16 v[98:99], v184 offset:0xe00
	v_mfma_f32_32x32x16_f16 v[32:47], v[4:7], v[100:103], v[32:47]
	ds_read_b64_tr_b16 v[100:101], v184 offset:0x1600
	ds_read_b64_tr_b16 v[102:103], v184 offset:0x1e00
	v_mfma_f32_32x32x16_f16 v[32:47], v[8:11], v[104:107], v[32:47]
	ds_read_b64_tr_b16 v[104:105], v184 offset:0x2600
	ds_read_b64_tr_b16 v[106:107], v184 offset:0x2e00
	ds_read_b64_tr_b16 v[112:113], v184 offset:0x3600
	ds_read_b64_tr_b16 v[114:115], v184 offset:0x3e00
	v_mfma_f32_32x32x16_f16 v[32:47], v[12:15], v[108:111], v[32:47]
	s_waitcnt lgkmcnt(0)
	v_mfma_f32_32x32x16_f16 v[16:31], v[0:3], v[96:99], v[16:31]
	s_nop 10
	v_mov_b64_e32 v[158:159], v[46:47]
	v_mov_b64_e32 v[142:143], v[62:63]
	v_mov_b64_e32 v[156:157], v[44:45]
	v_mov_b64_e32 v[154:155], v[42:43]
	v_mov_b64_e32 v[152:153], v[40:41]
	v_mov_b64_e32 v[150:151], v[38:39]
	v_mov_b64_e32 v[148:149], v[36:37]
	v_mfma_f32_32x32x16_f16 v[16:31], v[4:7], v[100:103], v[16:31]
	v_mov_b64_e32 v[146:147], v[34:35]
	v_mov_b64_e32 v[144:145], v[32:33]
	v_mov_b64_e32 v[140:141], v[60:61]
	v_mov_b64_e32 v[138:139], v[58:59]
	v_mov_b64_e32 v[136:137], v[56:57]
	v_mov_b64_e32 v[134:135], v[54:55]
	v_mov_b64_e32 v[132:133], v[52:53]
	v_mfma_f32_32x32x16_f16 v[16:31], v[8:11], v[104:107], v[16:31]
	v_mov_b64_e32 v[130:131], v[50:51]
	v_mov_b64_e32 v[128:129], v[48:49]
	v_mfma_f32_32x32x16_f16 v[16:31], v[12:15], v[112:115], v[16:31]
	v_mov_b64_e32 v[126:127], v[78:79]
	v_mov_b64_e32 v[0:1], v[80:81]
	v_mov_b64_e32 v[124:125], v[76:77]
	v_mov_b64_e32 v[122:123], v[74:75]
	v_mov_b64_e32 v[120:121], v[72:73]
	v_mov_b64_e32 v[118:119], v[70:71]
	v_mov_b64_e32 v[116:117], v[68:69]
	s_nop 4
	v_mov_b64_e32 v[174:175], v[30:31]
	v_mov_b64_e32 v[114:115], v[66:67]
	v_mov_b64_e32 v[112:113], v[64:65]
	v_mov_b64_e32 v[172:173], v[28:29]
	v_mov_b64_e32 v[170:171], v[26:27]
	v_mov_b64_e32 v[168:169], v[24:25]
	v_mov_b64_e32 v[166:167], v[22:23]
	v_mov_b64_e32 v[164:165], v[20:21]
	v_mov_b64_e32 v[162:163], v[18:19]
	v_mov_b64_e32 v[160:161], v[16:17]
	v_mov_b64_e32 v[2:3], v[82:83]
	v_mov_b64_e32 v[4:5], v[84:85]
	v_mov_b64_e32 v[6:7], v[86:87]
	v_mov_b64_e32 v[8:9], v[88:89]
	v_mov_b64_e32 v[10:11], v[90:91]
	v_mov_b64_e32 v[12:13], v[92:93]
	v_mov_b64_e32 v[14:15], v[94:95]

.LBB3_44:
	s_mov_b32 s5, s99
	s_mov_b32 m0, s86
	s_add_i32 s6, s4, 0xffff2000
	ds_read_b128 v[0:3], v190 offset:32768
	ds_read_b128 v[82:85], v190 offset:40960
	buffer_load_dwordx4 v191, s[68:71], s6 offen lds
	ds_read_b128 v[4:7], v189 offset:32768
	ds_read_b128 v[86:89], v189 offset:40960
	s_add_i32 s7, s4, 0xffff4000
	s_mov_b32 m0, s85
	s_waitcnt lgkmcnt(3)
	v_mfma_f32_32x32x16_f16 v[112:127], v[0:3], v[156:159], -0.5
	s_add_i32 s8, s4, 0xffff6000
	buffer_load_dwordx4 v191, s[68:71], s7 offen lds
	s_waitcnt lgkmcnt(1)
	v_mfma_f32_32x32x16_f16 v[112:127], v[4:7], v[152:155], v[112:127]
	v_mfma_f32_32x32x16_f16 v[0:15], v[82:85], v[156:159], -0.5
	ds_read_b128 v[82:85], v188 offset:32768
	s_mov_b32 m0, s84
	s_add_i32 s9, s4, 0xffff8000
	s_add_i32 s10, s4, 0xfffea000
	v_add_f32_e32 v81, 0, v169
	v_add_f32_e32 v81, v170, v81
	s_waitcnt lgkmcnt(1)
	v_mfma_f32_32x32x16_f16 v[0:15], v[86:89], v[152:155], v[0:15]
	ds_read_b128 v[86:89], v188 offset:40960
	buffer_load_dwordx4 v191, s[68:71], s8 offen lds
	s_mov_b32 m0, s83
	v_add_f32_e32 v81, v171, v81
	v_add_f32_e32 v81, v172, v81
	v_add_f32_e32 v81, v173, v81
	v_add_f32_e32 v81, v174, v81
	s_waitcnt lgkmcnt(1)
	v_mfma_f32_32x32x16_f16 v[112:127], v[82:85], v[148:151], v[112:127]
	ds_read_b128 v[82:85], v187 offset:32768
	ds_read_b128 v[90:93], v187 offset:40960
	buffer_load_dwordx4 v191, s[68:71], s9 offen lds
	s_mov_b32 m0, s90
	ds_read_b128 v[160:163], v190 offset:32896
	ds_read_b128 v[164:167], v190 offset:41088
	buffer_load_dwordx4 v186, s[72:75], s10 offen lds
	s_add_i32 s10, s4, 0xfffec000
	s_mov_b32 m0, s89
	s_waitcnt lgkmcnt(4)
	v_mfma_f32_32x32x16_f16 v[0:15], v[86:89], v[148:151], v[0:15]
	ds_read_b128 v[86:89], v189 offset:32896
	ds_read_b128 v[192:195], v189 offset:41088
	buffer_load_dwordx4 v186, s[72:75], s10 offen lds
	s_add_i32 s10, s4, 0xfffee000
	s_mov_b32 m0, s88
	v_add_f32_e32 v81, v175, v81
	v_add_f32_e32 v81, v176, v81
	v_add_f32_e32 v81, v177, v81
	s_waitcnt lgkmcnt(5)
	v_mfma_f32_32x32x16_f16 v[112:127], v[82:85], v[144:147], v[112:127]
	ds_read_b128 v[82:85], v188 offset:32896
	ds_read_b128 v[196:199], v188 offset:41088
	buffer_load_dwordx4 v186, s[72:75], s10 offen lds
	s_add_i32 s10, s4, 0xffff0000
	s_mov_b32 m0, s87
	ds_read_b128 v[200:203], v187 offset:32896
	ds_read_b128 v[204:207], v187 offset:41088
	buffer_load_dwordx4 v186, s[72:75], s10 offen lds
	v_add_f32_e32 v81, v178, v81
	s_waitcnt lgkmcnt(8)
	v_mfma_f32_32x32x16_f16 v[0:15], v[90:93], v[144:147], v[0:15]
	v_add_f32_e32 v81, v179, v81
	v_add_f32_e32 v81, v180, v81
	v_exp_f32_e32 v90, v96
	v_add_f32_e32 v81, v181, v81
	v_exp_f32_e32 v91, v97
	v_add_f32_e32 v81, v182, v81
	v_exp_f32_e32 v92, v98
	s_waitcnt lgkmcnt(6)
	v_mfma_f32_32x32x16_f16 v[0:15], v[164:167], v[140:143], v[0:15]
	v_add_f32_e32 v81, v183, v81
	v_exp_f32_e32 v93, v99
	v_add_f32_e32 v81, v185, v81
	v_exp_f32_e32 v94, v100
	v_add_f32_e32 v81, v90, v81
	v_exp_f32_e32 v95, v101
	v_add_f32_e32 v81, v91, v81
	v_mfma_f32_32x32x16_f16 v[112:127], v[160:163], v[140:143], v[112:127]
	v_exp_f32_e32 v96, v102
	v_add_f32_e32 v81, v92, v81
	v_exp_f32_e32 v97, v103
	v_add_f32_e32 v81, v93, v81
	v_exp_f32_e32 v98, v104
	v_add_f32_e32 v81, v94, v81
	v_exp_f32_e32 v99, v105
	s_waitcnt lgkmcnt(4)
	v_mfma_f32_32x32x16_f16 v[0:15], v[192:195], v[136:139], v[0:15]
	v_add_f32_e32 v81, v95, v81
	v_exp_f32_e32 v100, v106
	v_add_f32_e32 v81, v96, v81
	v_exp_f32_e32 v101, v107
	v_add_f32_e32 v81, v97, v81
	v_exp_f32_e32 v102, v108
	v_add_f32_e32 v81, v98, v81
	v_mfma_f32_32x32x16_f16 v[112:127], v[86:89], v[136:139], v[112:127]
	v_exp_f32_e32 v103, v109
	v_add_f32_e32 v81, v99, v81
	v_exp_f32_e32 v104, v110
	v_add_f32_e32 v81, v100, v81
	v_exp_f32_e32 v105, v111
	v_add_f32_e32 v81, v101, v81
	v_add_f32_e32 v81, v102, v81
	s_waitcnt lgkmcnt(2)
	v_mfma_f32_32x32x16_f16 v[0:15], v[196:199], v[132:135], v[0:15]
	v_add_f32_e32 v81, v103, v81
	v_add_f32_e32 v81, v104, v81
	v_add_f32_e32 v81, v105, v81
	v_cvt_pk_f16_f32 v86, v181, v182
	v_cvt_pk_f16_f32 v87, v183, v185
	v_cvt_pk_f16_f32 v88, v90, v91
	v_cvt_pk_f16_f32 v89, v92, v93
	v_mfma_f32_32x32x16_f16 v[112:127], v[82:85], v[132:135], v[112:127]
	v_mov_b32_e32 v82, v81
	s_nop 1
	v_permlane32_swap_b32_e32 v81, v82
	v_add_f32_e32 v81, v81, v82
	v_add_f32_e32 v209, v80, v81
	v_cvt_pk_f16_f32 v80, v169, v170
	v_cvt_pk_f16_f32 v82, v173, v174
	s_waitcnt lgkmcnt(0)
	v_mfma_f32_32x32x16_f16 v[0:15], v[204:207], v[128:131], v[0:15]
	v_cvt_pk_f16_f32 v81, v171, v172
	v_cvt_pk_f16_f32 v83, v175, v176
	v_permlane32_swap_b32_e32 v80, v82
	v_cvt_pk_f16_f32 v84, v177, v178
	v_cvt_pk_f16_f32 v85, v179, v180
	v_cvt_pk_f16_f32 v90, v94, v95
	v_cvt_pk_f16_f32 v91, v96, v97
	v_cvt_pk_f16_f32 v92, v98, v99
	v_cvt_pk_f16_f32 v93, v100, v101
	v_cvt_pk_f16_f32 v94, v102, v103
	v_cvt_pk_f16_f32 v95, v104, v105
	v_mfma_f32_32x32x16_f16 v[112:127], v[200:203], v[128:131], v[112:127]
	v_permlane32_swap_b32_e32 v81, v83
	v_permlane32_swap_b32_e32 v84, v86
	v_permlane32_swap_b32_e32 v85, v87
	v_permlane32_swap_b32_e32 v88, v90
	v_permlane32_swap_b32_e32 v89, v91
	v_permlane32_swap_b32_e32 v92, v94
	v_permlane32_swap_b32_e32 v93, v95
	ds_read_b64_tr_b16 v[96:97], v184 offset:0
	ds_read_b64_tr_b16 v[98:99], v184 offset:0x800
	ds_read_b64_tr_b16 v[100:101], v184 offset:0x1000
	ds_read_b64_tr_b16 v[102:103], v184 offset:0x1800
	ds_read_b64_tr_b16 v[104:105], v184 offset:0x2000
	ds_read_b64_tr_b16 v[106:107], v184 offset:0x2800
	ds_read_b64_tr_b16 v[108:109], v184 offset:0x3000
	ds_read_b64_tr_b16 v[110:111], v184 offset:0x3800
	s_waitcnt lgkmcnt(0)
	s_nop 0
	v_mfma_f32_32x32x16_f16 v[64:79], v[80:83], v[96:99], v[64:79]
	ds_read_b64_tr_b16 v[96:97], v184 offset:0x200
	ds_read_b64_tr_b16 v[98:99], v184 offset:0xa00
	s_nop 2
	v_exp_f32_e32 v208, v112
	v_exp_f32_e32 v192, v113
	v_exp_f32_e32 v193, v114
	v_exp_f32_e32 v194, v115
	v_mfma_f32_32x32x16_f16 v[64:79], v[84:87], v[100:103], v[64:79]
	ds_read_b64_tr_b16 v[100:101], v184 offset:0x1200
	ds_read_b64_tr_b16 v[102:103], v184 offset:0x1a00
	v_mfma_f32_32x32x16_f16 v[64:79], v[88:91], v[104:107], v[64:79]
	ds_read_b64_tr_b16 v[104:105], v184 offset:0x2200
	ds_read_b64_tr_b16 v[106:107], v184 offset:0x2a00
	ds_read_b64_tr_b16 v[112:113], v184 offset:0x3200
	ds_read_b64_tr_b16 v[114:115], v184 offset:0x3a00
	v_mfma_f32_32x32x16_f16 v[64:79], v[92:95], v[108:111], v[64:79]
	s_waitcnt lgkmcnt(0)
	v_mfma_f32_32x32x16_f16 v[48:63], v[80:83], v[96:99], v[48:63]
	ds_read_b64_tr_b16 v[96:97], v184 offset:0x400
	ds_read_b64_tr_b16 v[98:99], v184 offset:0xc00
	v_exp_f32_e32 v195, v116
	v_exp_f32_e32 v196, v117
	v_exp_f32_e32 v197, v118
	v_exp_f32_e32 v198, v119
	v_mfma_f32_32x32x16_f16 v[48:63], v[84:87], v[100:103], v[48:63]
	ds_read_b64_tr_b16 v[100:101], v184 offset:0x1400
	ds_read_b64_tr_b16 v[102:103], v184 offset:0x1c00
	v_mfma_f32_32x32x16_f16 v[48:63], v[88:91], v[104:107], v[48:63]
	ds_read_b64_tr_b16 v[104:105], v184 offset:0x2400
	ds_read_b64_tr_b16 v[106:107], v184 offset:0x2c00
	ds_read_b64_tr_b16 v[108:109], v184 offset:0x3400
	ds_read_b64_tr_b16 v[110:111], v184 offset:0x3c00
	v_mfma_f32_32x32x16_f16 v[48:63], v[92:95], v[112:115], v[48:63]
	s_waitcnt lgkmcnt(0)
	v_mfma_f32_32x32x16_f16 v[32:47], v[80:83], v[96:99], v[32:47]
	ds_read_b64_tr_b16 v[96:97], v184 offset:0x600
	ds_read_b64_tr_b16 v[98:99], v184 offset:0xe00
	v_exp_f32_e32 v199, v120
	v_exp_f32_e32 v200, v121
	v_exp_f32_e32 v201, v122
	v_exp_f32_e32 v202, v123
	v_mfma_f32_32x32x16_f16 v[32:47], v[84:87], v[100:103], v[32:47]
	ds_read_b64_tr_b16 v[100:101], v184 offset:0x1600
	ds_read_b64_tr_b16 v[102:103], v184 offset:0x1e00
	v_mfma_f32_32x32x16_f16 v[32:47], v[88:91], v[104:107], v[32:47]
	ds_read_b64_tr_b16 v[104:105], v184 offset:0x2600
	ds_read_b64_tr_b16 v[106:107], v184 offset:0x2e00
	ds_read_b64_tr_b16 v[112:113], v184 offset:0x3600
	ds_read_b64_tr_b16 v[114:115], v184 offset:0x3e00
	v_mfma_f32_32x32x16_f16 v[32:47], v[92:95], v[108:111], v[32:47]
	s_waitcnt lgkmcnt(0)
	v_mfma_f32_32x32x16_f16 v[16:31], v[80:83], v[96:99], v[16:31]
	v_exp_f32_e32 v203, v124
	v_exp_f32_e32 v204, v125
	v_exp_f32_e32 v205, v126
	v_exp_f32_e32 v206, v127
	s_waitcnt vmcnt(0) lgkmcnt(0)
	s_barrier
	v_mfma_f32_32x32x16_f16 v[16:31], v[84:87], v[100:103], v[16:31]
	v_mfma_f32_32x32x16_f16 v[16:31], v[88:91], v[104:107], v[16:31]
	v_mfma_f32_32x32x16_f16 v[16:31], v[92:95], v[112:115], v[16:31]
	s_mov_b32 m0, s91
	s_add_i32 s10, s4, 0xffffa000
	ds_read_b128 v[80:83], v190
	ds_read_b128 v[84:87], v190 offset:8192
	buffer_load_dwordx4 v191, s[68:71], s10 offen lds
	ds_read_b128 v[88:91], v189
	ds_read_b128 v[92:95], v189 offset:8192
	s_add_i32 s10, s4, 0xffffc000
	s_mov_b32 m0, s92
	s_waitcnt lgkmcnt(3)
	v_mfma_f32_32x32x16_f16 v[112:127], v[80:83], v[156:159], -0.5
	s_waitcnt lgkmcnt(2)
	v_mfma_f32_32x32x16_f16 v[96:111], v[84:87], v[156:159], -0.5
	v_exp_f32_e32 v0, v0
	buffer_load_dwordx4 v191, s[68:71], s10 offen lds
	ds_read_b128 v[80:83], v188
	ds_read_b128 v[84:87], v188 offset:8192
	s_waitcnt lgkmcnt(3)
	v_mfma_f32_32x32x16_f16 v[112:127], v[88:91], v[152:155], v[112:127]
	s_add_i32 s10, s4, 0xffffe000
	s_mov_b32 m0, s93
	v_exp_f32_e32 v1, v1
	buffer_load_dwordx4 v191, s[68:71], s10 offen lds
	s_mov_b32 m0, s94
	v_exp_f32_e32 v2, v2
	v_exp_f32_e32 v3, v3
	s_waitcnt lgkmcnt(2)
	v_mfma_f32_32x32x16_f16 v[96:111], v[92:95], v[152:155], v[96:111]
	v_exp_f32_e32 v4, v4
	v_exp_f32_e32 v5, v5
	v_exp_f32_e32 v6, v6
	v_exp_f32_e32 v7, v7
	v_exp_f32_e32 v8, v8
	v_exp_f32_e32 v9, v9
	v_exp_f32_e32 v10, v10
	s_waitcnt lgkmcnt(1)
	v_mfma_f32_32x32x16_f16 v[112:127], v[80:83], v[148:151], v[112:127]
	ds_read_b128 v[80:83], v187
	ds_read_b128 v[88:91], v187 offset:8192
	buffer_load_dwordx4 v191, s[68:71], s4 offen lds
	s_mov_b32 m0, s3
	ds_read_b128 v[92:95], v190 offset:128
	ds_read_b128 v[160:163], v190 offset:8320
	buffer_load_dwordx4 v186, s[72:75], s6 offen lds
	s_mov_b32 m0, s82
	v_exp_f32_e32 v11, v11
	s_waitcnt lgkmcnt(4)
	v_mfma_f32_32x32x16_f16 v[96:111], v[84:87], v[148:151], v[96:111]
	ds_read_b128 v[84:87], v189 offset:128
	ds_read_b128 v[164:167], v189 offset:8320
	buffer_load_dwordx4 v186, s[72:75], s7 offen lds
	s_mov_b32 m0, s81
	ds_read_b128 v[170:173], v188 offset:128
	ds_read_b128 v[174:177], v188 offset:8320
	buffer_load_dwordx4 v186, s[72:75], s8 offen lds
	s_mov_b32 m0, s80
	v_exp_f32_e32 v12, v12
	s_waitcnt lgkmcnt(7)
	v_mfma_f32_32x32x16_f16 v[112:127], v[80:83], v[144:147], v[112:127]
	ds_read_b128 v[80:83], v187 offset:128
	ds_read_b128 v[178:181], v187 offset:8320
	buffer_load_dwordx4 v186, s[72:75], s9 offen lds
	v_exp_f32_e32 v13, v13
	v_exp_f32_e32 v14, v14
	v_exp_f32_e32 v15, v15
	s_waitcnt lgkmcnt(8)
	v_mfma_f32_32x32x16_f16 v[96:111], v[88:91], v[144:147], v[96:111]
	v_add_f32_e32 v88, 0, v208
	v_add_f32_e32 v88, v192, v88
	v_add_f32_e32 v88, v193, v88
	v_add_f32_e32 v88, v194, v88
	v_add_f32_e32 v88, v195, v88
	v_add_f32_e32 v88, v196, v88
	v_add_f32_e32 v88, v197, v88
	s_waitcnt lgkmcnt(7)
	v_mfma_f32_32x32x16_f16 v[112:127], v[92:95], v[140:143], v[112:127]
	v_add_f32_e32 v88, v198, v88
	v_cvt_pk_f16_f32 v89, v205, v206
	v_cvt_pk_f16_f32 v90, v0, v1
	v_cvt_pk_f16_f32 v91, v2, v3
	v_cvt_pk_f16_f32 v92, v4, v5
	v_cvt_pk_f16_f32 v93, v6, v7
	s_nop 0
	v_permlane32_swap_b32_e32 v90, v92
	s_waitcnt lgkmcnt(6)
	v_mfma_f32_32x32x16_f16 v[96:111], v[160:163], v[140:143], v[96:111]
	v_cvt_pk_f16_f32 v160, v8, v9
	v_cvt_pk_f16_f32 v161, v10, v11
	v_cvt_pk_f16_f32 v162, v12, v13
	v_cvt_pk_f16_f32 v163, v14, v15
	v_permlane32_swap_b32_e32 v91, v93
	v_permlane32_swap_b32_e32 v160, v162
	s_waitcnt lgkmcnt(5)
	v_mfma_f32_32x32x16_f16 v[112:127], v[84:87], v[136:139], v[112:127]
	v_add_f32_e32 v84, v199, v88
	v_add_f32_e32 v84, v200, v84
	v_add_f32_e32 v84, v201, v84
	v_add_f32_e32 v84, v202, v84
	v_add_f32_e32 v84, v203, v84
	v_add_f32_e32 v84, v204, v84
	v_add_f32_e32 v84, v205, v84
	s_waitcnt lgkmcnt(4)
	v_mfma_f32_32x32x16_f16 v[96:111], v[164:167], v[136:139], v[96:111]
	v_add_f32_e32 v84, v206, v84
	v_add_f32_e32 v84, v0, v84
	v_add_f32_e32 v84, v1, v84
	v_add_f32_e32 v84, v2, v84
	v_add_f32_e32 v84, v3, v84
	v_add_f32_e32 v84, v4, v84
	v_add_f32_e32 v84, v5, v84
	s_waitcnt lgkmcnt(2)
	v_mfma_f32_32x32x16_f16 v[96:111], v[174:177], v[132:135], v[96:111]
	v_add_f32_e32 v84, v6, v84
	v_add_f32_e32 v84, v7, v84
	v_add_f32_e32 v84, v8, v84
	v_add_f32_e32 v84, v9, v84
	v_add_f32_e32 v84, v10, v84
	v_add_f32_e32 v84, v11, v84
	v_add_f32_e32 v84, v12, v84
	v_mfma_f32_32x32x16_f16 v[112:127], v[170:173], v[132:135], v[112:127]
	v_add_f32_e32 v84, v13, v84
	v_add_f32_e32 v84, v14, v84
	v_add_f32_e32 v84, v15, v84
	v_mov_b32_e32 v85, v84
	s_nop 1
	v_permlane32_swap_b32_e32 v84, v85
	v_add_f32_e32 v84, v84, v85
	s_waitcnt lgkmcnt(0)
	v_mfma_f32_32x32x16_f16 v[96:111], v[178:181], v[128:131], v[96:111]
	v_cvt_pk_f16_f32 v85, v197, v198
	v_cvt_pk_f16_f32 v86, v199, v200
	v_cvt_pk_f16_f32 v87, v201, v202
	v_cvt_pk_f16_f32 v88, v203, v204
	s_nop 1
	v_permlane32_swap_b32_e32 v86, v88
	v_permlane32_swap_b32_e32 v87, v89
	v_mfma_f32_32x32x16_f16 v[112:127], v[80:83], v[128:131], v[112:127]
	v_add_f32_e32 v80, v209, v84
	v_cvt_pk_f16_f32 v82, v208, v192
	v_cvt_pk_f16_f32 v83, v193, v194
	v_cvt_pk_f16_f32 v84, v195, v196
	s_nop 1
	v_permlane32_swap_b32_e32 v82, v84
	v_permlane32_swap_b32_e32 v83, v85
	v_permlane32_swap_b32_e32 v161, v163
	ds_read_b64_tr_b16 v[164:165], v184 offset:0x8000
	ds_read_b64_tr_b16 v[166:167], v184 offset:0x8800
	ds_read_b64_tr_b16 v[170:171], v184 offset:0x9000
	ds_read_b64_tr_b16 v[172:173], v184 offset:0x9800
	ds_read_b64_tr_b16 v[174:175], v184 offset:0xa000
	ds_read_b64_tr_b16 v[176:177], v184 offset:0xa800
	ds_read_b64_tr_b16 v[178:179], v184 offset:0xb000
	ds_read_b64_tr_b16 v[180:181], v184 offset:0xb800
	s_waitcnt lgkmcnt(0)
	s_nop 0
	v_mfma_f32_32x32x16_f16 v[64:79], v[82:85], v[164:167], v[64:79]
	s_nop 0
	v_exp_f32_e32 v169, v112
	v_mfma_f32_32x32x16_f16 v[64:79], v[86:89], v[170:173], v[64:79]
	v_exp_f32_e32 v170, v113
	ds_read_b64_tr_b16 v[112:113], v184 offset:0x8200
	v_exp_f32_e32 v171, v114
	v_exp_f32_e32 v172, v115
	ds_read_b64_tr_b16 v[114:115], v184 offset:0x8a00
	ds_read_b64_tr_b16 v[164:165], v184 offset:0x9200
	ds_read_b64_tr_b16 v[166:167], v184 offset:0x9a00
	v_mfma_f32_32x32x16_f16 v[64:79], v[90:93], v[174:177], v[64:79]
	ds_read_b64_tr_b16 v[210:211], v184 offset:0xa200
	ds_read_b64_tr_b16 v[212:213], v184 offset:0xaa00
	ds_read_b64_tr_b16 v[214:215], v184 offset:0xb200
	ds_read_b64_tr_b16 v[216:217], v184 offset:0xba00
	v_mfma_f32_32x32x16_f16 v[64:79], v[160:163], v[178:181], v[64:79]
	s_waitcnt lgkmcnt(0)
	v_mfma_f32_32x32x16_f16 v[48:63], v[82:85], v[112:115], v[48:63]
	ds_read_b64_tr_b16 v[112:113], v184 offset:0x8400
	ds_read_b64_tr_b16 v[114:115], v184 offset:0x8c00
	v_exp_f32_e32 v173, v116
	v_exp_f32_e32 v174, v117
	ds_read_b64_tr_b16 v[116:117], v184 offset:0x9400
	v_exp_f32_e32 v175, v118
	v_exp_f32_e32 v176, v119
	v_mfma_f32_32x32x16_f16 v[48:63], v[86:89], v[164:167], v[48:63]
	ds_read_b64_tr_b16 v[118:119], v184 offset:0x9c00
	ds_read_b64_tr_b16 v[164:165], v184 offset:0xa400
	ds_read_b64_tr_b16 v[166:167], v184 offset:0xac00
	v_mfma_f32_32x32x16_f16 v[48:63], v[90:93], v[210:213], v[48:63]
	ds_read_b64_tr_b16 v[210:211], v184 offset:0xb400
	ds_read_b64_tr_b16 v[212:213], v184 offset:0xbc00
	v_mfma_f32_32x32x16_f16 v[48:63], v[160:163], v[214:217], v[48:63]
	s_waitcnt lgkmcnt(0)
	v_mfma_f32_32x32x16_f16 v[32:47], v[82:85], v[112:115], v[32:47]
	ds_read_b64_tr_b16 v[112:113], v184 offset:0x8600
	ds_read_b64_tr_b16 v[114:115], v184 offset:0x8e00
	v_exp_f32_e32 v177, v120
	v_exp_f32_e32 v178, v121
	v_exp_f32_e32 v179, v122
	v_exp_f32_e32 v180, v123
	v_mfma_f32_32x32x16_f16 v[32:47], v[86:89], v[116:119], v[32:47]
	ds_read_b64_tr_b16 v[116:117], v184 offset:0x9600
	ds_read_b64_tr_b16 v[118:119], v184 offset:0x9e00
	ds_read_b64_tr_b16 v[120:121], v184 offset:0xa600
	ds_read_b64_tr_b16 v[122:123], v184 offset:0xae00
	v_mfma_f32_32x32x16_f16 v[32:47], v[90:93], v[164:167], v[32:47]
	ds_read_b64_tr_b16 v[164:165], v184 offset:0xb600
	ds_read_b64_tr_b16 v[166:167], v184 offset:0xbe00
	v_mfma_f32_32x32x16_f16 v[32:47], v[160:163], v[210:213], v[32:47]
	s_waitcnt lgkmcnt(0)
	v_mfma_f32_32x32x16_f16 v[16:31], v[82:85], v[112:115], v[16:31]
	v_exp_f32_e32 v181, v124
	v_exp_f32_e32 v182, v125
	v_exp_f32_e32 v183, v126
	v_exp_f32_e32 v185, v127
	s_waitcnt vmcnt(0) lgkmcnt(0)
	s_barrier
	v_mfma_f32_32x32x16_f16 v[16:31], v[86:89], v[116:119], v[16:31]
	v_mfma_f32_32x32x16_f16 v[16:31], v[90:93], v[120:123], v[16:31]
	v_mfma_f32_32x32x16_f16 v[16:31], v[160:163], v[164:167], v[16:31]
	s_add_i32 s99, s99, 2
	s_add_i32 s4, s4, 0x10000
	s_add_i32 s5, s5, 4
	s_cmp_le_u32 s5, s33
	s_cbranch_scc1 .LBB3_44
	s_cmp_gt_u32 s99, s33
	s_cbranch_scc0 .LBB3_47
	s_branch .LBB3_60

.LBB3_59:
	ds_read_b64_tr_b16 v[164:165], v184 offset:0
	ds_read_b64_tr_b16 v[166:167], v184 offset:0x800
	ds_read_b64_tr_b16 v[192:193], v184 offset:0x1000
	ds_read_b64_tr_b16 v[194:195], v184 offset:0x1800
	ds_read_b64_tr_b16 v[196:197], v184 offset:0x2000
	ds_read_b64_tr_b16 v[198:199], v184 offset:0x2800
	ds_read_b64_tr_b16 v[200:201], v184 offset:0x3000
	ds_read_b64_tr_b16 v[202:203], v184 offset:0x3800
	s_waitcnt lgkmcnt(0)
	v_add_f32_e32 v81, v81, v94
	v_add_f32_e32 v80, v80, v81
	v_mfma_f32_32x32x16_f16 v[64:79], v[82:85], v[164:167], v[64:79]
	v_exp_f32_e32 v208, v112
	v_mfma_f32_32x32x16_f16 v[64:79], v[90:93], v[192:195], v[64:79]
	v_exp_f32_e32 v192, v113
	ds_read_b64_tr_b16 v[112:113], v184 offset:0x200
	v_exp_f32_e32 v193, v114
	v_exp_f32_e32 v194, v115
	ds_read_b64_tr_b16 v[114:115], v184 offset:0xa00
	ds_read_b64_tr_b16 v[164:165], v184 offset:0x1200
	ds_read_b64_tr_b16 v[166:167], v184 offset:0x1a00
	v_mfma_f32_32x32x16_f16 v[64:79], v[160:163], v[196:199], v[64:79]
	ds_read_b64_tr_b16 v[204:205], v184 offset:0x2200
	ds_read_b64_tr_b16 v[206:207], v184 offset:0x2a00
	ds_read_b64_tr_b16 v[210:211], v184 offset:0x3200
	ds_read_b64_tr_b16 v[212:213], v184 offset:0x3a00
	v_mfma_f32_32x32x16_f16 v[64:79], v[86:89], v[200:203], v[64:79]
	s_waitcnt lgkmcnt(0)
	v_mfma_f32_32x32x16_f16 v[48:63], v[82:85], v[112:115], v[48:63]
	ds_read_b64_tr_b16 v[112:113], v184 offset:0x400
	ds_read_b64_tr_b16 v[114:115], v184 offset:0xc00
	v_exp_f32_e32 v195, v116
	v_exp_f32_e32 v196, v117
	ds_read_b64_tr_b16 v[116:117], v184 offset:0x1400
	v_exp_f32_e32 v197, v118
	v_exp_f32_e32 v198, v119
	v_mfma_f32_32x32x16_f16 v[48:63], v[90:93], v[164:167], v[48:63]
	ds_read_b64_tr_b16 v[118:119], v184 offset:0x1c00
	ds_read_b64_tr_b16 v[164:165], v184 offset:0x2400
	ds_read_b64_tr_b16 v[166:167], v184 offset:0x2c00
	v_mfma_f32_32x32x16_f16 v[48:63], v[160:163], v[204:207], v[48:63]
	ds_read_b64_tr_b16 v[204:205], v184 offset:0x3400
	ds_read_b64_tr_b16 v[206:207], v184 offset:0x3c00
	v_mfma_f32_32x32x16_f16 v[48:63], v[86:89], v[210:213], v[48:63]
	s_waitcnt lgkmcnt(0)
	v_mfma_f32_32x32x16_f16 v[32:47], v[82:85], v[112:115], v[32:47]
	ds_read_b64_tr_b16 v[112:113], v184 offset:0x600
	ds_read_b64_tr_b16 v[114:115], v184 offset:0xe00
	v_exp_f32_e32 v199, v120
	v_exp_f32_e32 v200, v121
	v_exp_f32_e32 v201, v122
	v_exp_f32_e32 v202, v123
	v_mfma_f32_32x32x16_f16 v[32:47], v[90:93], v[116:119], v[32:47]
	ds_read_b64_tr_b16 v[116:117], v184 offset:0x1600
	ds_read_b64_tr_b16 v[118:119], v184 offset:0x1e00
	ds_read_b64_tr_b16 v[120:121], v184 offset:0x2600
	ds_read_b64_tr_b16 v[122:123], v184 offset:0x2e00
	v_mfma_f32_32x32x16_f16 v[32:47], v[160:163], v[164:167], v[32:47]
	ds_read_b64_tr_b16 v[164:165], v184 offset:0x3600
	ds_read_b64_tr_b16 v[166:167], v184 offset:0x3e00
	v_mfma_f32_32x32x16_f16 v[32:47], v[86:89], v[204:207], v[32:47]
	s_waitcnt lgkmcnt(0)
	v_mfma_f32_32x32x16_f16 v[16:31], v[82:85], v[112:115], v[16:31]
	v_exp_f32_e32 v203, v124
	v_exp_f32_e32 v204, v125
	v_exp_f32_e32 v205, v126
	v_exp_f32_e32 v206, v127
	s_waitcnt vmcnt(0) lgkmcnt(0)
	s_barrier
	v_mfma_f32_32x32x16_f16 v[16:31], v[90:93], v[116:119], v[16:31]
	v_mfma_f32_32x32x16_f16 v[16:31], v[160:163], v[120:123], v[16:31]
	v_mfma_f32_32x32x16_f16 v[16:31], v[86:89], v[164:167], v[16:31]
.LBB3_60:
	s_cmp_ge_u32 s99, s33
	v_cvt_pk_f16_f32 v164, v208, v192
	v_cvt_pk_f16_f32 v165, v193, v194
	v_cvt_pk_f16_f32 v166, v195, v196
	v_cvt_pk_f16_f32 v167, v197, v198
	v_cvt_pk_f16_f32 v160, v199, v200
	v_cvt_pk_f16_f32 v161, v201, v202
	v_cvt_pk_f16_f32 v162, v203, v204
	v_cvt_pk_f16_f32 v163, v205, v206
	v_add_f32_e32 v81, 0, v208
	s_cbranch_scc1 .LBB3_62
	ds_read_b128 v[82:85], v189
	ds_read_b128 v[86:89], v190
	ds_read_b128 v[114:117], v189 offset:8192
	ds_read_b128 v[118:121], v190 offset:128
	ds_read_b128 v[122:125], v190 offset:8192
	ds_read_b128 v[170:173], v190 offset:8320
	s_mov_b32 m0, s3
	s_waitcnt lgkmcnt(4)
	v_mfma_f32_32x32x16_f16 v[98:113], v[86:89], v[156:159], -0.5
	s_lshl_b32 s3, s99, 15
	v_mfma_f32_32x32x16_f16 v[98:113], v[82:85], v[152:155], v[98:113]
	s_waitcnt lgkmcnt(1)
	v_mfma_f32_32x32x16_f16 v[82:97], v[122:125], v[156:159], -0.5
	ds_read_b128 v[122:125], v188 offset:8192
	ds_read_b128 v[156:159], v188
	s_add_i32 s4, s3, 0x8000
	s_mov_b32 s74, s70
	s_mov_b32 s75, s71
	v_exp_f32_e32 v0, v0
	v_exp_f32_e32 v1, v1
	v_mfma_f32_32x32x16_f16 v[82:97], v[114:117], v[152:155], v[82:97]
	ds_read_b128 v[114:117], v187 offset:8192
	ds_read_b128 v[152:155], v187
	buffer_load_dwordx4 v186, s[72:75], s4 offen lds
	s_add_i32 s4, s3, 0xa000
	s_mov_b32 m0, s82
	v_exp_f32_e32 v2, v2
	v_exp_f32_e32 v3, v3
	v_exp_f32_e32 v4, v4
	s_waitcnt lgkmcnt(2)
	v_mfma_f32_32x32x16_f16 v[98:113], v[156:159], v[148:151], v[98:113]
	ds_read_b128 v[156:159], v189 offset:8320
	ds_read_b128 v[174:177], v189 offset:128
	buffer_load_dwordx4 v186, s[72:75], s4 offen lds
	s_add_i32 s4, s3, 0xc000
	s_mov_b32 m0, s81
	ds_read_b128 v[178:181], v188 offset:8320
	ds_read_b128 v[188:191], v188 offset:128
	buffer_load_dwordx4 v186, s[72:75], s4 offen lds
	s_add_i32 s3, s3, 0xe000
	s_mov_b32 m0, s80
	v_mfma_f32_32x32x16_f16 v[82:97], v[122:125], v[148:151], v[82:97]
	ds_read_b128 v[122:125], v187 offset:8320
	ds_read_b128 v[148:151], v187 offset:128
	buffer_load_dwordx4 v186, s[72:75], s3 offen lds
	v_exp_f32_e32 v5, v5
	v_exp_f32_e32 v6, v6
	v_exp_f32_e32 v7, v7
	v_exp_f32_e32 v8, v8
	v_exp_f32_e32 v9, v9
	s_waitcnt lgkmcnt(6)
	v_mfma_f32_32x32x16_f16 v[98:113], v[152:155], v[144:147], v[98:113]
	v_exp_f32_e32 v10, v10
	v_exp_f32_e32 v11, v11
	v_exp_f32_e32 v12, v12
	v_exp_f32_e32 v13, v13
	v_exp_f32_e32 v14, v14
	v_exp_f32_e32 v15, v15
	v_cvt_pk_f16_f32 v126, v0, v1
	v_mfma_f32_32x32x16_f16 v[82:97], v[114:117], v[144:147], v[82:97]
	v_add_f32_e32 v114, v192, v81
	v_add_f32_e32 v114, v193, v114
	v_add_f32_e32 v114, v194, v114
	v_add_f32_e32 v114, v195, v114
	v_add_f32_e32 v114, v196, v114
	v_add_f32_e32 v114, v197, v114
	v_add_f32_e32 v114, v198, v114
	v_mfma_f32_32x32x16_f16 v[98:113], v[118:121], v[140:143], v[98:113]
	v_add_f32_e32 v114, v199, v114
	v_add_f32_e32 v114, v200, v114
	v_add_f32_e32 v114, v201, v114
	v_add_f32_e32 v114, v202, v114
	v_add_f32_e32 v114, v203, v114
	v_add_f32_e32 v114, v204, v114
	v_add_f32_e32 v114, v205, v114
	v_mfma_f32_32x32x16_f16 v[82:97], v[170:173], v[140:143], v[82:97]
	v_add_f32_e32 v114, v206, v114
	v_add_f32_e32 v114, v0, v114
	v_add_f32_e32 v114, v1, v114
	v_add_f32_e32 v114, v2, v114
	v_add_f32_e32 v114, v3, v114
	v_add_f32_e32 v114, v4, v114
	v_add_f32_e32 v114, v5, v114
	s_waitcnt lgkmcnt(4)
	v_mfma_f32_32x32x16_f16 v[98:113], v[174:177], v[136:139], v[98:113]
	v_add_f32_e32 v114, v6, v114
	v_add_f32_e32 v114, v7, v114
	v_add_f32_e32 v114, v8, v114
	v_add_f32_e32 v114, v9, v114
	v_add_f32_e32 v114, v10, v114
	v_add_f32_e32 v114, v11, v114
	v_add_f32_e32 v114, v12, v114
	v_mfma_f32_32x32x16_f16 v[82:97], v[156:159], v[136:139], v[82:97]
	v_add_f32_e32 v114, v13, v114
	v_add_f32_e32 v114, v14, v114
	v_add_f32_e32 v114, v15, v114
	v_mov_b32_e32 v115, v114
	s_nop 1
	v_permlane32_swap_b32_e32 v114, v115
	v_add_f32_e32 v114, v114, v115
	s_waitcnt lgkmcnt(2)
	v_mfma_f32_32x32x16_f16 v[98:113], v[188:191], v[132:135], v[98:113]
	v_add_f32_e32 v80, v80, v114
	v_mov_b32_e32 v114, v164
	v_mov_b32_e32 v116, v166
	v_mov_b32_e32 v115, v165
	v_mov_b32_e32 v117, v167
	v_mov_b32_e32 v118, v160
	v_mov_b32_e32 v120, v162
	v_mfma_f32_32x32x16_f16 v[82:97], v[178:181], v[132:135], v[82:97]
	v_mov_b32_e32 v119, v161
	v_mov_b32_e32 v121, v163
	v_cvt_pk_f16_f32 v127, v2, v3
	v_permlane32_swap_b32_e32 v114, v116
	v_permlane32_swap_b32_e32 v115, v117
	s_waitcnt lgkmcnt(0)
	v_mfma_f32_32x32x16_f16 v[98:113], v[148:151], v[128:131], v[98:113]
	v_permlane32_swap_b32_e32 v118, v120
	v_permlane32_swap_b32_e32 v119, v121
	v_mfma_f32_32x32x16_f16 v[82:97], v[122:125], v[128:131], v[82:97]
	v_cvt_pk_f16_f32 v128, v4, v5
	v_cvt_pk_f16_f32 v129, v6, v7
	v_cvt_pk_f16_f32 v122, v8, v9
	v_cvt_pk_f16_f32 v123, v10, v11
	v_cvt_pk_f16_f32 v124, v12, v13
	v_cvt_pk_f16_f32 v125, v14, v15
	v_permlane32_swap_b32_e32 v126, v128
	v_permlane32_swap_b32_e32 v127, v129
	v_permlane32_swap_b32_e32 v122, v124
	v_permlane32_swap_b32_e32 v123, v125
	s_lshl_b32 s3, s99, 7
	v_subrev_u32_e32 v130, s3, v168
	v_add_u32_e32 v130, 0xffffff80, v130
	v_mov_b32_e32 v131, 0xff800000
	v_cmp_gt_i32_e64 s[60:61], 26, v130
	v_cmp_gt_i32_e64 s[64:65], 27, v130
	v_cmp_gt_i32_e64 s[58:59], 25, v130
	s_and_b64 s[60:61], s[64:65], s[60:61]
	v_cmp_gt_i32_e64 s[56:57], 24, v130
	s_and_b64 s[58:59], s[60:61], s[58:59]
	v_cmp_gt_i32_e64 s[54:55], 19, v130
	s_and_b64 s[56:57], s[58:59], s[56:57]
	v_cmp_gt_i32_e64 s[52:53], 18, v130
	s_and_b64 s[54:55], s[56:57], s[54:55]
	v_cmp_gt_i32_e64 s[50:51], 17, v130
	s_and_b64 s[52:53], s[54:55], s[52:53]
	v_cmp_gt_i32_e64 s[48:49], 16, v130
	s_and_b64 s[50:51], s[52:53], s[50:51]
	v_cmp_gt_i32_e64 s[46:47], 11, v130
	s_and_b64 s[48:49], s[50:51], s[48:49]
	v_cmp_gt_i32_e64 s[44:45], 10, v130
	s_and_b64 s[46:47], s[48:49], s[46:47]
	v_cmp_gt_i32_e64 s[42:43], 9, v130
	s_and_b64 s[44:45], s[46:47], s[44:45]
	v_cmp_gt_i32_e64 s[40:41], 8, v130
	s_and_b64 s[42:43], s[44:45], s[42:43]
	v_cmp_gt_i32_e64 s[38:39], 3, v130
	s_and_b64 s[40:41], s[42:43], s[40:41]
	v_cmp_gt_i32_e64 s[36:37], 2, v130
	s_and_b64 s[38:39], s[40:41], s[38:39]
	v_cmp_gt_i32_e64 s[34:35], 1, v130
	s_and_b64 s[36:37], s[38:39], s[36:37]
	v_cmp_gt_i32_e64 s[30:31], 0, v130
	s_and_b64 s[34:35], s[36:37], s[34:35]
	s_and_b64 s[30:31], s[34:35], s[30:31]
	v_cmp_gt_i32_e64 s[62:63], 58, v130
	v_cndmask_b32_e64 v137, v98, v131, s[30:31]
	v_cmp_gt_i32_e64 s[30:31], 59, v130
	v_cmp_gt_i32_e64 s[26:27], 57, v130
	v_cndmask_b32_e64 v138, v111, v131, s[58:59]
	v_cndmask_b32_e64 v111, v97, v131, s[30:31]
	s_and_b64 s[30:31], s[30:31], s[62:63]
	v_cmp_gt_i32_e64 s[24:25], 56, v130
	s_and_b64 s[26:27], s[30:31], s[26:27]
	v_cmp_gt_i32_e64 s[22:23], 51, v130
	s_and_b64 s[24:25], s[26:27], s[24:25]
	v_cmp_gt_i32_e64 s[20:21], 50, v130
	s_and_b64 s[22:23], s[24:25], s[22:23]
	v_cmp_gt_i32_e64 s[18:19], 49, v130
	s_and_b64 s[20:21], s[22:23], s[20:21]
	v_cmp_gt_i32_e64 s[16:17], 48, v130
	s_and_b64 s[18:19], s[20:21], s[18:19]
	v_cmp_gt_i32_e64 s[14:15], 43, v130
	s_and_b64 s[16:17], s[18:19], s[16:17]
	v_cmp_gt_i32_e64 s[12:13], 42, v130
	s_and_b64 s[14:15], s[16:17], s[14:15]
	v_cmp_gt_i32_e64 s[10:11], 41, v130
	s_and_b64 s[12:13], s[14:15], s[12:13]
	v_cmp_gt_i32_e64 s[8:9], 40, v130
	s_and_b64 s[10:11], s[12:13], s[10:11]
	v_cmp_gt_i32_e64 s[6:7], 35, v130
	s_and_b64 s[8:9], s[10:11], s[8:9]
	v_cmp_gt_i32_e64 s[4:5], 34, v130
	s_and_b64 s[6:7], s[8:9], s[6:7]
	v_cmp_gt_i32_e64 s[28:29], 33, v130
	s_and_b64 s[4:5], s[6:7], s[4:5]
	v_cmp_gt_i32_e32 vcc, 32, v130
	v_cndmask_b32_e64 v98, v84, v131, s[4:5]
	s_and_b64 s[4:5], s[4:5], s[28:29]
	s_and_b64 vcc, s[4:5], vcc
	v_cndmask_b32_e64 v139, v110, v131, s[56:57]
	v_cndmask_b32_e64 v110, v96, v131, s[30:31]
	v_cndmask_b32_e64 v97, v83, v131, s[4:5]
	v_cndmask_b32_e32 v96, v82, v131, vcc
	ds_read_b64_tr_b16 v[82:83], v184 offset:0x8000
	v_cndmask_b32_e64 v136, v99, v131, s[34:35]
	v_cndmask_b32_e64 v99, v85, v131, s[6:7]
	ds_read_b64_tr_b16 v[84:85], v184 offset:0x8800
	v_cndmask_b32_e64 v134, v101, v131, s[38:39]
	v_cndmask_b32_e64 v135, v100, v131, s[36:37]
	v_cndmask_b32_e64 v101, v87, v131, s[10:11]
	v_cndmask_b32_e64 v100, v86, v131, s[8:9]
	ds_read_b64_tr_b16 v[86:87], v184 offset:0x9000
	v_cndmask_b32_e64 v146, v103, v131, s[42:43]
	v_cndmask_b32_e64 v147, v102, v131, s[40:41]
	v_cndmask_b32_e64 v103, v89, v131, s[14:15]
	v_cndmask_b32_e64 v102, v88, v131, s[12:13]
	ds_read_b64_tr_b16 v[88:89], v184 offset:0x9800
	v_cndmask_b32_e64 v144, v105, v131, s[46:47]
	v_cndmask_b32_e64 v145, v104, v131, s[44:45]
	v_cndmask_b32_e64 v105, v91, v131, s[18:19]
	v_cndmask_b32_e64 v104, v90, v131, s[16:17]
	ds_read_b64_tr_b16 v[90:91], v184 offset:0xa000
	v_cndmask_b32_e64 v142, v107, v131, s[50:51]
	v_cndmask_b32_e64 v143, v106, v131, s[48:49]
	v_cndmask_b32_e64 v107, v93, v131, s[22:23]
	v_cndmask_b32_e64 v106, v92, v131, s[20:21]
	ds_read_b64_tr_b16 v[92:93], v184 offset:0xa800
	v_cndmask_b32_e64 v113, v113, v131, s[64:65]
	v_cndmask_b32_e64 v112, v112, v131, s[60:61]
	v_cndmask_b32_e64 v140, v109, v131, s[54:55]
	v_cndmask_b32_e64 v141, v108, v131, s[52:53]
	v_cndmask_b32_e64 v109, v95, v131, s[26:27]
	v_cndmask_b32_e64 v108, v94, v131, s[24:25]
	ds_read_b64_tr_b16 v[130:131], v184 offset:0xb000
	ds_read_b64_tr_b16 v[132:133], v184 offset:0xb800
	s_waitcnt lgkmcnt(0)
	v_mfma_f32_32x32x16_f16 v[64:79], v[114:117], v[82:85], v[64:79]
	ds_read_b64_tr_b16 v[82:83], v184 offset:0x8200
	ds_read_b64_tr_b16 v[84:85], v184 offset:0x8a00
	v_exp_f32_e32 v171, v135
	v_exp_f32_e32 v172, v134
	v_exp_f32_e32 v169, v137
	v_exp_f32_e32 v170, v136
	v_mfma_f32_32x32x16_f16 v[64:79], v[118:121], v[86:89], v[64:79]
	ds_read_b64_tr_b16 v[86:87], v184 offset:0x9200
	ds_read_b64_tr_b16 v[88:89], v184 offset:0x9a00
	v_mfma_f32_32x32x16_f16 v[64:79], v[126:129], v[90:93], v[64:79]
	ds_read_b64_tr_b16 v[90:91], v184 offset:0xa200
	ds_read_b64_tr_b16 v[92:93], v184 offset:0xaa00
	ds_read_b64_tr_b16 v[134:135], v184 offset:0xb200
	ds_read_b64_tr_b16 v[136:137], v184 offset:0xba00
	v_mfma_f32_32x32x16_f16 v[64:79], v[122:125], v[130:133], v[64:79]
	s_waitcnt lgkmcnt(0)
	v_mfma_f32_32x32x16_f16 v[48:63], v[114:117], v[82:85], v[48:63]
	ds_read_b64_tr_b16 v[82:83], v184 offset:0x8400
	ds_read_b64_tr_b16 v[84:85], v184 offset:0x8c00
	v_exp_f32_e32 v173, v147
	v_exp_f32_e32 v174, v146
	v_exp_f32_e32 v175, v145
	v_exp_f32_e32 v176, v144
	v_mfma_f32_32x32x16_f16 v[48:63], v[118:121], v[86:89], v[48:63]
	ds_read_b64_tr_b16 v[86:87], v184 offset:0x9400
	ds_read_b64_tr_b16 v[88:89], v184 offset:0x9c00
	v_mfma_f32_32x32x16_f16 v[48:63], v[126:129], v[90:93], v[48:63]
	ds_read_b64_tr_b16 v[90:91], v184 offset:0xa400
	ds_read_b64_tr_b16 v[92:93], v184 offset:0xac00
	ds_read_b64_tr_b16 v[130:131], v184 offset:0xb400
	ds_read_b64_tr_b16 v[132:133], v184 offset:0xbc00
	v_mfma_f32_32x32x16_f16 v[48:63], v[122:125], v[134:137], v[48:63]
	s_waitcnt lgkmcnt(0)
	v_mfma_f32_32x32x16_f16 v[32:47], v[114:117], v[82:85], v[32:47]
	ds_read_b64_tr_b16 v[82:83], v184 offset:0x8600
	ds_read_b64_tr_b16 v[84:85], v184 offset:0x8e00
	v_exp_f32_e32 v177, v143
	v_exp_f32_e32 v178, v142
	v_exp_f32_e32 v179, v141
	v_exp_f32_e32 v180, v140
	v_mfma_f32_32x32x16_f16 v[32:47], v[118:121], v[86:89], v[32:47]
	ds_read_b64_tr_b16 v[86:87], v184 offset:0x9600
	ds_read_b64_tr_b16 v[88:89], v184 offset:0x9e00
	v_mfma_f32_32x32x16_f16 v[32:47], v[126:129], v[90:93], v[32:47]
	ds_read_b64_tr_b16 v[90:91], v184 offset:0xa600
	ds_read_b64_tr_b16 v[92:93], v184 offset:0xae00
	ds_read_b64_tr_b16 v[134:135], v184 offset:0xb600
	ds_read_b64_tr_b16 v[136:137], v184 offset:0xbe00
	v_mfma_f32_32x32x16_f16 v[32:47], v[122:125], v[130:133], v[32:47]
	s_waitcnt lgkmcnt(0)
	v_mfma_f32_32x32x16_f16 v[16:31], v[114:117], v[82:85], v[16:31]
	v_exp_f32_e32 v181, v139
	v_exp_f32_e32 v182, v138
	v_exp_f32_e32 v183, v112
	v_exp_f32_e32 v185, v113
	s_waitcnt vmcnt(0) lgkmcnt(0)
	s_barrier
	v_mfma_f32_32x32x16_f16 v[16:31], v[118:121], v[86:89], v[16:31]
	v_mfma_f32_32x32x16_f16 v[16:31], v[126:129], v[90:93], v[16:31]
	v_mfma_f32_32x32x16_f16 v[16:31], v[122:125], v[134:137], v[16:31]
.LBB3_62:
	s_bitcmp0_b32 s2, 3
	s_cbranch_scc1 .LBB3_64
	v_add_f32_e32 v81, v192, v81
	v_add_f32_e32 v81, v193, v81
	v_add_f32_e32 v81, v194, v81
	v_add_f32_e32 v81, v195, v81
	v_add_f32_e32 v81, v196, v81
	v_add_f32_e32 v81, v197, v81
	v_add_f32_e32 v81, v198, v81
	v_add_f32_e32 v81, v199, v81
	v_add_f32_e32 v81, v200, v81
	v_add_f32_e32 v81, v201, v81
	v_add_f32_e32 v81, v202, v81
	v_exp_f32_e32 v0, v0
	v_add_f32_e32 v81, v203, v81
	v_exp_f32_e32 v1, v1
	v_add_f32_e32 v81, v204, v81
	v_exp_f32_e32 v2, v2
	v_add_f32_e32 v81, v205, v81
	v_exp_f32_e32 v3, v3
	v_add_f32_e32 v81, v206, v81
	v_exp_f32_e32 v4, v4
	v_add_f32_e32 v81, v81, v0
	v_exp_f32_e32 v5, v5
	v_add_f32_e32 v81, v1, v81
	v_exp_f32_e32 v6, v6
	v_add_f32_e32 v81, v2, v81
	v_exp_f32_e32 v7, v7
	v_add_f32_e32 v81, v3, v81
	v_exp_f32_e32 v8, v8
	v_add_f32_e32 v81, v4, v81
	v_exp_f32_e32 v9, v9
	v_add_f32_e32 v81, v5, v81
	v_exp_f32_e32 v10, v10
	v_add_f32_e32 v81, v6, v81
	v_exp_f32_e32 v11, v11
	v_add_f32_e32 v81, v7, v81
	v_exp_f32_e32 v12, v12
	v_add_f32_e32 v81, v8, v81
	v_exp_f32_e32 v13, v13
	v_add_f32_e32 v81, v9, v81
	v_exp_f32_e32 v14, v14
	v_add_f32_e32 v81, v10, v81
	v_exp_f32_e32 v15, v15
	v_add_f32_e32 v81, v11, v81
	v_add_f32_e32 v81, v12, v81
	v_add_f32_e32 v81, v13, v81
	v_add_f32_e32 v81, v14, v81
	v_add_f32_e32 v81, v15, v81
	v_mov_b32_e32 v82, v81
	s_nop 1
	v_permlane32_swap_b32_e32 v81, v82
	v_add_f32_e32 v81, v81, v82
	v_cvt_pk_f16_f32 v82, v0, v1
	v_cvt_pk_f16_f32 v83, v2, v3
	v_cvt_pk_f16_f32 v84, v4, v5
	v_cvt_pk_f16_f32 v85, v6, v7
	v_cvt_pk_f16_f32 v86, v8, v9
	v_cvt_pk_f16_f32 v87, v10, v11
	v_cvt_pk_f16_f32 v88, v12, v13
	v_cvt_pk_f16_f32 v89, v14, v15
	v_permlane32_swap_b32_e32 v164, v166
	v_permlane32_swap_b32_e32 v165, v167
	v_permlane32_swap_b32_e32 v160, v162
	v_permlane32_swap_b32_e32 v161, v163
	v_permlane32_swap_b32_e32 v82, v84
	v_permlane32_swap_b32_e32 v83, v85
	v_permlane32_swap_b32_e32 v86, v88
	v_permlane32_swap_b32_e32 v87, v89
	ds_read_b64_tr_b16 v[90:91], v184 offset:0x8000
	ds_read_b64_tr_b16 v[92:93], v184 offset:0x8800
	ds_read_b64_tr_b16 v[112:113], v184 offset:0x9000
	ds_read_b64_tr_b16 v[114:115], v184 offset:0x9800
	ds_read_b64_tr_b16 v[116:117], v184 offset:0xa000
	ds_read_b64_tr_b16 v[118:119], v184 offset:0xa800
	ds_read_b64_tr_b16 v[120:121], v184 offset:0xb000
	ds_read_b64_tr_b16 v[122:123], v184 offset:0xb800
	s_waitcnt lgkmcnt(0)
	s_nop 0
	v_mfma_f32_32x32x16_f16 v[0:15], v[164:167], v[90:93], v[64:79]
	ds_read_b64_tr_b16 v[90:91], v184 offset:0x8200
	ds_read_b64_tr_b16 v[92:93], v184 offset:0x8a00
	ds_read_b64_tr_b16 v[128:129], v184 offset:0x9200
	ds_read_b64_tr_b16 v[130:131], v184 offset:0x9a00
	ds_read_b64_tr_b16 v[132:133], v184 offset:0xa200
	ds_read_b64_tr_b16 v[134:135], v184 offset:0xaa00
	ds_read_b64_tr_b16 v[136:137], v184 offset:0xb200
	v_mfma_f32_32x32x16_f16 v[0:15], v[160:163], v[112:115], v[0:15]
	ds_read_b64_tr_b16 v[138:139], v184 offset:0xba00
	v_mfma_f32_32x32x16_f16 v[0:15], v[82:85], v[116:119], v[0:15]
	v_mfma_f32_32x32x16_f16 v[0:15], v[86:89], v[120:123], v[0:15]
	s_waitcnt lgkmcnt(0)
	v_mfma_f32_32x32x16_f16 v[112:127], v[164:167], v[90:93], v[48:63]
	ds_read_b64_tr_b16 v[90:91], v184 offset:0x8400
	ds_read_b64_tr_b16 v[92:93], v184 offset:0x8c00
	ds_read_b64_tr_b16 v[144:145], v184 offset:0x9400
	ds_read_b64_tr_b16 v[146:147], v184 offset:0x9c00
	ds_read_b64_tr_b16 v[148:149], v184 offset:0xa400
	ds_read_b64_tr_b16 v[150:151], v184 offset:0xac00
	ds_read_b64_tr_b16 v[152:153], v184 offset:0xb400
	v_mfma_f32_32x32x16_f16 v[112:127], v[160:163], v[128:131], v[112:127]
	ds_read_b64_tr_b16 v[154:155], v184 offset:0xbc00
	v_mfma_f32_32x32x16_f16 v[112:127], v[82:85], v[132:135], v[112:127]
	v_mfma_f32_32x32x16_f16 v[112:127], v[86:89], v[136:139], v[112:127]
	s_waitcnt lgkmcnt(0)
	v_mfma_f32_32x32x16_f16 v[128:143], v[164:167], v[90:93], v[32:47]
	ds_read_b64_tr_b16 v[90:91], v184 offset:0x8600
	ds_read_b64_tr_b16 v[92:93], v184 offset:0x8e00
	ds_read_b64_tr_b16 v[186:187], v184 offset:0x9600
	ds_read_b64_tr_b16 v[188:189], v184 offset:0x9e00
	ds_read_b64_tr_b16 v[190:191], v184 offset:0xa600
	ds_read_b64_tr_b16 v[192:193], v184 offset:0xae00
	ds_read_b64_tr_b16 v[194:195], v184 offset:0xb600
	v_mfma_f32_32x32x16_f16 v[128:143], v[160:163], v[144:147], v[128:143]
	ds_read_b64_tr_b16 v[196:197], v184 offset:0xbe00
	v_mfma_f32_32x32x16_f16 v[128:143], v[82:85], v[148:151], v[128:143]
	v_mfma_f32_32x32x16_f16 v[128:143], v[86:89], v[152:155], v[128:143]
	s_waitcnt lgkmcnt(0)
	v_mfma_f32_32x32x16_f16 v[144:159], v[164:167], v[90:93], v[16:31]
	v_mfma_f32_32x32x16_f16 v[144:159], v[160:163], v[186:189], v[144:159]
	v_mfma_f32_32x32x16_f16 v[144:159], v[82:85], v[190:193], v[144:159]
	v_mfma_f32_32x32x16_f16 v[144:159], v[86:89], v[194:197], v[144:159]
	s_cbranch_execz .LBB3_65
	s_branch .LBB3_66
.LBB3_64:
.LBB3_65:
	v_add_f32_e32 v0, 0, v169
	v_add_f32_e32 v0, v170, v0
	v_add_f32_e32 v0, v171, v0
	v_add_f32_e32 v0, v172, v0
	v_add_f32_e32 v0, v173, v0
	v_add_f32_e32 v0, v174, v0
	v_add_f32_e32 v0, v175, v0
	v_add_f32_e32 v0, v176, v0
	v_add_f32_e32 v0, v177, v0
	v_add_f32_e32 v0, v178, v0
	v_add_f32_e32 v0, v179, v0
	v_add_f32_e32 v0, v180, v0
	v_exp_f32_e32 v8, v96
	v_add_f32_e32 v0, v181, v0
	v_exp_f32_e32 v9, v97
	v_add_f32_e32 v0, v182, v0
	v_exp_f32_e32 v10, v98
	v_add_f32_e32 v0, v183, v0
	v_exp_f32_e32 v11, v99
	v_add_f32_e32 v0, v185, v0
	v_exp_f32_e32 v12, v100
	v_add_f32_e32 v0, v8, v0
	v_exp_f32_e32 v13, v101
	v_add_f32_e32 v0, v9, v0
	v_exp_f32_e32 v14, v102
	v_add_f32_e32 v0, v10, v0
	v_exp_f32_e32 v15, v103
	v_add_f32_e32 v0, v11, v0
	v_exp_f32_e32 v82, v104
	v_add_f32_e32 v0, v12, v0
	v_exp_f32_e32 v83, v105
	v_add_f32_e32 v0, v13, v0
	v_exp_f32_e32 v84, v106
	v_add_f32_e32 v0, v14, v0
	v_exp_f32_e32 v85, v107
	v_add_f32_e32 v0, v15, v0
	v_exp_f32_e32 v86, v108
	v_add_f32_e32 v0, v82, v0
	v_exp_f32_e32 v87, v109
	v_add_f32_e32 v0, v83, v0
	v_exp_f32_e32 v88, v110
	v_add_f32_e32 v0, v84, v0
	v_exp_f32_e32 v89, v111
	v_add_f32_e32 v0, v85, v0
	v_add_f32_e32 v0, v86, v0
	v_add_f32_e32 v0, v87, v0
	v_add_f32_e32 v0, v88, v0
	v_add_f32_e32 v0, v89, v0
	v_mov_b32_e32 v1, v0
	s_nop 1
	v_permlane32_swap_b32_e32 v0, v1
	v_add_f32_e32 v81, v0, v1
	v_cvt_pk_f16_f32 v0, v169, v170
	v_cvt_pk_f16_f32 v1, v171, v172
	v_cvt_pk_f16_f32 v2, v173, v174
	v_cvt_pk_f16_f32 v3, v175, v176
	v_cvt_pk_f16_f32 v4, v177, v178
	v_cvt_pk_f16_f32 v5, v179, v180
	v_cvt_pk_f16_f32 v6, v181, v182
	v_cvt_pk_f16_f32 v7, v183, v185
	v_cvt_pk_f16_f32 v8, v8, v9
	v_cvt_pk_f16_f32 v9, v10, v11
	v_cvt_pk_f16_f32 v10, v12, v13
	v_cvt_pk_f16_f32 v11, v14, v15
	v_cvt_pk_f16_f32 v12, v82, v83
	v_cvt_pk_f16_f32 v13, v84, v85
	v_cvt_pk_f16_f32 v14, v86, v87
	v_cvt_pk_f16_f32 v15, v88, v89
	v_permlane32_swap_b32_e32 v0, v2
	v_permlane32_swap_b32_e32 v1, v3
	v_permlane32_swap_b32_e32 v4, v6
	v_permlane32_swap_b32_e32 v5, v7
	v_permlane32_swap_b32_e32 v8, v10
	v_permlane32_swap_b32_e32 v9, v11
	v_permlane32_swap_b32_e32 v12, v14
	v_permlane32_swap_b32_e32 v13, v15
	ds_read_b64_tr_b16 v[82:83], v184 offset:0
	ds_read_b64_tr_b16 v[84:85], v184 offset:0x800
	ds_read_b64_tr_b16 v[86:87], v184 offset:0x1000
	ds_read_b64_tr_b16 v[88:89], v184 offset:0x1800
	ds_read_b64_tr_b16 v[90:91], v184 offset:0x2000
	ds_read_b64_tr_b16 v[92:93], v184 offset:0x2800
	ds_read_b64_tr_b16 v[94:95], v184 offset:0x3000
	ds_read_b64_tr_b16 v[96:97], v184 offset:0x3800
	s_waitcnt lgkmcnt(0)
	s_nop 0
	v_mfma_f32_32x32x16_f16 v[64:79], v[0:3], v[82:85], v[64:79]
	ds_read_b64_tr_b16 v[82:83], v184 offset:0x200
	ds_read_b64_tr_b16 v[84:85], v184 offset:0xa00
	v_mfma_f32_32x32x16_f16 v[64:79], v[4:7], v[86:89], v[64:79]
	ds_read_b64_tr_b16 v[86:87], v184 offset:0x1200
	ds_read_b64_tr_b16 v[88:89], v184 offset:0x1a00
	v_mfma_f32_32x32x16_f16 v[64:79], v[8:11], v[90:93], v[64:79]
	ds_read_b64_tr_b16 v[90:91], v184 offset:0x2200
	ds_read_b64_tr_b16 v[92:93], v184 offset:0x2a00
	ds_read_b64_tr_b16 v[98:99], v184 offset:0x3200
	ds_read_b64_tr_b16 v[100:101], v184 offset:0x3a00
	v_mfma_f32_32x32x16_f16 v[64:79], v[12:15], v[94:97], v[64:79]
	s_waitcnt lgkmcnt(0)
	v_mfma_f32_32x32x16_f16 v[48:63], v[0:3], v[82:85], v[48:63]
	ds_read_b64_tr_b16 v[82:83], v184 offset:0x400
	ds_read_b64_tr_b16 v[84:85], v184 offset:0xc00
	v_mfma_f32_32x32x16_f16 v[48:63], v[4:7], v[86:89], v[48:63]
	ds_read_b64_tr_b16 v[86:87], v184 offset:0x1400
	ds_read_b64_tr_b16 v[88:89], v184 offset:0x1c00
	v_mfma_f32_32x32x16_f16 v[48:63], v[8:11], v[90:93], v[48:63]
	ds_read_b64_tr_b16 v[90:91], v184 offset:0x2400
	ds_read_b64_tr_b16 v[92:93], v184 offset:0x2c00
	ds_read_b64_tr_b16 v[94:95], v184 offset:0x3400
	ds_read_b64_tr_b16 v[96:97], v184 offset:0x3c00
	v_mfma_f32_32x32x16_f16 v[48:63], v[12:15], v[98:101], v[48:63]
	s_waitcnt lgkmcnt(0)
	v_mfma_f32_32x32x16_f16 v[32:47], v[0:3], v[82:85], v[32:47]
	ds_read_b64_tr_b16 v[82:83], v184 offset:0x600
	ds_read_b64_tr_b16 v[84:85], v184 offset:0xe00
	v_mfma_f32_32x32x16_f16 v[32:47], v[4:7], v[86:89], v[32:47]
	ds_read_b64_tr_b16 v[86:87], v184 offset:0x1600
	ds_read_b64_tr_b16 v[88:89], v184 offset:0x1e00
	v_mfma_f32_32x32x16_f16 v[32:47], v[8:11], v[90:93], v[32:47]
	ds_read_b64_tr_b16 v[90:91], v184 offset:0x2600
	ds_read_b64_tr_b16 v[92:93], v184 offset:0x2e00
	ds_read_b64_tr_b16 v[98:99], v184 offset:0x3600
	ds_read_b64_tr_b16 v[100:101], v184 offset:0x3e00
	v_mfma_f32_32x32x16_f16 v[32:47], v[12:15], v[94:97], v[32:47]
	s_waitcnt lgkmcnt(0)
	v_mfma_f32_32x32x16_f16 v[16:31], v[0:3], v[82:85], v[16:31]
	s_nop 10
	v_mov_b64_e32 v[142:143], v[46:47]
	v_mov_b64_e32 v[126:127], v[62:63]
	v_mov_b64_e32 v[140:141], v[44:45]
	v_mov_b64_e32 v[138:139], v[42:43]
	v_mov_b64_e32 v[136:137], v[40:41]
	v_mov_b64_e32 v[134:135], v[38:39]
	v_mov_b64_e32 v[132:133], v[36:37]
	v_mfma_f32_32x32x16_f16 v[16:31], v[4:7], v[86:89], v[16:31]
	v_mov_b64_e32 v[130:131], v[34:35]
	v_mov_b64_e32 v[128:129], v[32:33]
	v_mov_b64_e32 v[124:125], v[60:61]
	v_mov_b64_e32 v[122:123], v[58:59]
	v_mov_b64_e32 v[120:121], v[56:57]
	v_mov_b64_e32 v[118:119], v[54:55]
	v_mov_b64_e32 v[116:117], v[52:53]
	v_mfma_f32_32x32x16_f16 v[16:31], v[8:11], v[90:93], v[16:31]
	v_mov_b64_e32 v[114:115], v[50:51]
	v_mov_b64_e32 v[112:113], v[48:49]
	v_mfma_f32_32x32x16_f16 v[16:31], v[12:15], v[98:101], v[16:31]
	v_mov_b64_e32 v[0:1], v[64:65]
	v_mov_b64_e32 v[2:3], v[66:67]
	v_mov_b64_e32 v[4:5], v[68:69]
	v_mov_b64_e32 v[6:7], v[70:71]
	v_mov_b64_e32 v[8:9], v[72:73]
	v_mov_b64_e32 v[10:11], v[74:75]
	v_mov_b64_e32 v[12:13], v[76:77]
	s_nop 4
	v_mov_b64_e32 v[158:159], v[30:31]
	v_mov_b64_e32 v[156:157], v[28:29]
	v_mov_b64_e32 v[154:155], v[26:27]
	v_mov_b64_e32 v[152:153], v[24:25]
	v_mov_b64_e32 v[150:151], v[22:23]
	v_mov_b64_e32 v[148:149], v[20:21]
	v_mov_b64_e32 v[146:147], v[18:19]
	v_mov_b64_e32 v[144:145], v[16:17]
	v_mov_b64_e32 v[14:15], v[78:79]
